# k_phase epilogue: 8 bias loads hoisted to one burst + single vmcnt wait (v240-v255), on top of X-loader rewrite
# baseline (speedup 1.0000x reference)
.LBB2_7:
	s_and_b64 vcc, exec, s[12:13]
	s_cbranch_vccz .LBB2_10
	s_cmpk_lt_u32 s2, 0x80
	s_waitcnt lgkmcnt(0)
	s_cselect_b32 s5, s5, s7
	s_cselect_b32 s4, s4, s6
	s_lshl_b32 s6, s15, 20
	s_add_u32 s4, s4, s6
	s_addc_u32 s5, s5, 0
	s_lshl_b32 s6, s14, 2
	s_add_u32 s4, s4, s6
	s_addc_u32 s5, s5, 0
	s_lshl_b32 s6, s3, 5
	s_add_i32 s7, s6, 0xffffff80
	v_or_b32_e32 v2, s7, v1
	v_mov_b32_e32 v3, 0
	v_lshlrev_b64 v[4:5], 14, v[2:3]
	v_or_b32_e32 v133, 20, v2
	v_or_b32_e32 v137, 24, v2
	v_or_b32_e32 v138, 28, v2
	v_lshl_add_u32 v204, v132, 4, v4
	v_lshrrev_b32_e32 v132, 3, v132
	s_mov_b64 s[30:31], s[4:5]
	s_and_b32 s28, s2, 7
	s_lshr_b32 s29, s2, 6
	s_lshl_b32 s29, s29, 3
	s_or_b32 s28, s28, s29
	s_min_u32 s28, s28, 30
	s_lshl_b32 s28, s28, 8
	s_mov_b32 s28, 0
	v_add_u32_e32 v205, 0x10000, v204
	v_add_u32_e32 v206, 0x20000, v204
	v_add_u32_e32 v207, 0x30000, v204
	v_add_u32_e32 v208, 0x40000, v204
	v_add_u32_e32 v209, 0x50000, v204
	v_add_u32_e32 v210, 0x60000, v204
	v_add_u32_e32 v211, 0x70000, v204
	s_add_u32 s22, s30, s28
	s_addc_u32 s23, s31, 0
	global_load_dwordx4 v[2:5], v204, s[22:23] nt
	global_load_dwordx4 v[6:9], v205, s[22:23] nt
	global_load_dwordx4 v[10:13], v206, s[22:23] nt
	global_load_dwordx4 v[14:17], v207, s[22:23] nt
	global_load_dwordx4 v[18:21], v208, s[22:23] nt
	global_load_dwordx4 v[22:25], v209, s[22:23] nt
	global_load_dwordx4 v[26:29], v210, s[22:23] nt
	global_load_dwordx4 v[30:33], v211, s[22:23] nt
	s_addk_i32 s28, 0x100
	s_and_b32 s28, s28, 0x1fff
	s_add_u32 s22, s30, s28
	s_addc_u32 s23, s31, 0
	global_load_dwordx4 v[34:37], v204, s[22:23] nt
	global_load_dwordx4 v[38:41], v205, s[22:23] nt
	global_load_dwordx4 v[42:45], v206, s[22:23] nt
	global_load_dwordx4 v[46:49], v207, s[22:23] nt
	global_load_dwordx4 v[50:53], v208, s[22:23] nt
	global_load_dwordx4 v[54:57], v209, s[22:23] nt
	global_load_dwordx4 v[58:61], v210, s[22:23] nt
	global_load_dwordx4 v[62:65], v211, s[22:23] nt
	s_addk_i32 s28, 0x100
	s_and_b32 s28, s28, 0x1fff
	s_add_u32 s22, s30, s28
	s_addc_u32 s23, s31, 0
	global_load_dwordx4 v[66:69], v204, s[22:23] nt
	global_load_dwordx4 v[70:73], v205, s[22:23] nt
	global_load_dwordx4 v[74:77], v206, s[22:23] nt
	global_load_dwordx4 v[78:81], v207, s[22:23] nt
	global_load_dwordx4 v[82:85], v208, s[22:23] nt
	global_load_dwordx4 v[86:89], v209, s[22:23] nt
	global_load_dwordx4 v[90:93], v210, s[22:23] nt
	global_load_dwordx4 v[94:97], v211, s[22:23] nt
	s_addk_i32 s28, 0x100
	s_and_b32 s28, s28, 0x1fff
	s_add_u32 s22, s30, s28
	s_addc_u32 s23, s31, 0
	global_load_dwordx4 v[98:101], v204, s[22:23] nt
	global_load_dwordx4 v[102:105], v205, s[22:23] nt
	global_load_dwordx4 v[106:109], v206, s[22:23] nt
	global_load_dwordx4 v[110:113], v207, s[22:23] nt
	global_load_dwordx4 v[114:117], v208, s[22:23] nt
	global_load_dwordx4 v[118:121], v209, s[22:23] nt
	global_load_dwordx4 v[122:125], v210, s[22:23] nt
	global_load_dwordx4 v[126:129], v211, s[22:23] nt
	s_addk_i32 s28, 0x100
	s_and_b32 s28, s28, 0x1fff
	s_add_u32 s22, s30, s28
	s_addc_u32 s23, s31, 0
	global_load_dwordx4 v[140:143], v204, s[22:23] nt
	global_load_dwordx4 v[144:147], v205, s[22:23] nt
	global_load_dwordx4 v[148:151], v206, s[22:23] nt
	global_load_dwordx4 v[152:155], v207, s[22:23] nt
	global_load_dwordx4 v[156:159], v208, s[22:23] nt
	global_load_dwordx4 v[160:163], v209, s[22:23] nt
	global_load_dwordx4 v[164:167], v210, s[22:23] nt
	global_load_dwordx4 v[168:171], v211, s[22:23] nt
	s_addk_i32 s28, 0x100
	s_and_b32 s28, s28, 0x1fff
	s_add_u32 s22, s30, s28
	s_addc_u32 s23, s31, 0
	global_load_dwordx4 v[172:175], v204, s[22:23] nt
	global_load_dwordx4 v[176:179], v205, s[22:23] nt
	global_load_dwordx4 v[180:183], v206, s[22:23] nt
	global_load_dwordx4 v[184:187], v207, s[22:23] nt
	global_load_dwordx4 v[188:191], v208, s[22:23] nt
	global_load_dwordx4 v[192:195], v209, s[22:23] nt
	global_load_dwordx4 v[196:199], v210, s[22:23] nt
	global_load_dwordx4 v[200:203], v211, s[22:23] nt
	s_addk_i32 s28, 0x100
	s_and_b32 s28, s28, 0x1fff
	v_lshlrev_b32_e32 v135, 3, v0
	s_lshr_b32 s4, s7, 3
	s_addk_i32 s6, 0xff90
	v_and_b32_e32 v139, 56, v135
	v_or_b32_e32 v135, s4, v132
	s_lshr_b32 s4, s6, 3
	v_or_b32_e32 v136, s4, v132
	v_lshl_or_b32 v1, v1, 6, v139
	v_lshl_or_b32 v1, v136, 10, v1
	v_lshrrev_b32_e32 v136, 3, v133
	v_lshlrev_b32_e32 v133, 6, v133
	s_movk_i32 s4, 0x1c0
	v_or_b32_e32 v136, v136, v132
	v_and_or_b32 v133, v133, s4, v139
	v_lshl_or_b32 v133, v136, 10, v133
	v_add_u32_e32 v136, 0x18000, v133
	v_lshrrev_b32_e32 v133, 3, v137
	s_mov_b32 s4, 0x3ffffe
	v_and_or_b32 v133, v133, s4, v132
	v_lshlrev_b32_e32 v137, 6, v137
	v_and_b32_e32 v137, 0x2c0, v137
	v_lshlrev_b32_e32 v133, 10, v133
	v_or3_b32 v133, v133, v137, v139
	v_add_u32_e32 v133, 0x18000, v133
	v_lshrrev_b32_e32 v134, 4, v0
	v_xor_b32_e32 v137, 32, v133
	v_lshrrev_b32_e32 v133, 3, v138
	v_lshlrev_b32_e32 v134, 6, v134
	v_and_or_b32 v132, v133, s4, v132
	v_lshlrev_b32_e32 v133, 6, v138
	v_and_b32_e32 v134, 0xc0, v134
	v_lshlrev_b32_e32 v135, 10, v135
	v_and_b32_e32 v133, 0x3c0, v133
	v_lshlrev_b32_e32 v132, 10, v132
	v_or3_b32 v135, v135, v134, v139
	v_or3_b32 v132, v132, v133, v139
	v_add_u32_e32 v134, 0x18000, v135
	v_add_u32_e32 v132, 0x18000, v132
	v_add_u32_e32 v135, 0x18100, v135
	v_add_u32_e32 v1, 0x18000, v1
	v_xor_b32_e32 v138, 32, v132
	v_xor_b32_e32 v139, 32, v134
	s_waitcnt vmcnt(40)
	v_cvt_pk_f16_f32 v2, v2, v3
	v_cvt_pk_f16_f32 v3, v4, v5
	v_cvt_pk_f16_f32 v6, v6, v7
	v_cvt_pk_f16_f32 v7, v8, v9
	v_cvt_pk_f16_f32 v10, v10, v11
	v_cvt_pk_f16_f32 v11, v12, v13
	v_cvt_pk_f16_f32 v14, v14, v15
	v_cvt_pk_f16_f32 v15, v16, v17
	v_cvt_pk_f16_f32 v18, v18, v19
	v_cvt_pk_f16_f32 v19, v20, v21
	v_cvt_pk_f16_f32 v22, v22, v23
	v_cvt_pk_f16_f32 v23, v24, v25
	v_cvt_pk_f16_f32 v26, v26, v27
	v_cvt_pk_f16_f32 v27, v28, v29
	v_cvt_pk_f16_f32 v30, v30, v31
	v_cvt_pk_f16_f32 v31, v32, v33
	ds_write_b64 v134, v[2:3]
	ds_write_b64 v135, v[6:7]
	ds_write_b64 v139, v[10:11] offset:512
	ds_write_b64 v139, v[14:15] offset:768
	ds_write_b64 v1, v[18:19]
	ds_write_b64 v136, v[22:23]
	ds_write_b64 v137, v[26:27]
	ds_write_b64 v138, v[30:31]
	s_add_u32 s22, s30, s28
	s_addc_u32 s23, s31, 0
	global_load_dwordx4 v[2:5], v204, s[22:23] nt
	global_load_dwordx4 v[6:9], v205, s[22:23] nt
	global_load_dwordx4 v[10:13], v206, s[22:23] nt
	global_load_dwordx4 v[14:17], v207, s[22:23] nt
	global_load_dwordx4 v[18:21], v208, s[22:23] nt
	global_load_dwordx4 v[22:25], v209, s[22:23] nt
	global_load_dwordx4 v[26:29], v210, s[22:23] nt
	global_load_dwordx4 v[30:33], v211, s[22:23] nt
	s_addk_i32 s28, 0x100
	s_and_b32 s28, s28, 0x1fff
	s_waitcnt lgkmcnt(0)
	s_barrier
	s_waitcnt vmcnt(40)
	v_cvt_pk_f16_f32 v34, v34, v35
	v_cvt_pk_f16_f32 v35, v36, v37
	v_cvt_pk_f16_f32 v38, v38, v39
	v_cvt_pk_f16_f32 v39, v40, v41
	v_cvt_pk_f16_f32 v42, v42, v43
	v_cvt_pk_f16_f32 v43, v44, v45
	v_cvt_pk_f16_f32 v46, v46, v47
	v_cvt_pk_f16_f32 v47, v48, v49
	v_cvt_pk_f16_f32 v50, v50, v51
	v_cvt_pk_f16_f32 v51, v52, v53
	v_cvt_pk_f16_f32 v54, v54, v55
	v_cvt_pk_f16_f32 v55, v56, v57
	v_cvt_pk_f16_f32 v58, v58, v59
	v_cvt_pk_f16_f32 v59, v60, v61
	v_cvt_pk_f16_f32 v62, v62, v63
	v_cvt_pk_f16_f32 v63, v64, v65
	ds_write_b64 v134, v[34:35] offset:8192
	ds_write_b64 v135, v[38:39] offset:8192
	ds_write_b64 v139, v[42:43] offset:8704
	ds_write_b64 v139, v[46:47] offset:8960
	ds_write_b64 v1, v[50:51] offset:8192
	ds_write_b64 v136, v[54:55] offset:8192
	ds_write_b64 v137, v[58:59] offset:8192
	ds_write_b64 v138, v[62:63] offset:8192
	s_add_u32 s22, s30, s28
	s_addc_u32 s23, s31, 0
	global_load_dwordx4 v[34:37], v204, s[22:23] nt
	global_load_dwordx4 v[38:41], v205, s[22:23] nt
	global_load_dwordx4 v[42:45], v206, s[22:23] nt
	global_load_dwordx4 v[46:49], v207, s[22:23] nt
	global_load_dwordx4 v[50:53], v208, s[22:23] nt
	global_load_dwordx4 v[54:57], v209, s[22:23] nt
	global_load_dwordx4 v[58:61], v210, s[22:23] nt
	global_load_dwordx4 v[62:65], v211, s[22:23] nt
	s_addk_i32 s28, 0x100
	s_and_b32 s28, s28, 0x1fff
	s_waitcnt lgkmcnt(0)
	s_barrier
	s_waitcnt vmcnt(40)
	v_cvt_pk_f16_f32 v66, v66, v67
	v_cvt_pk_f16_f32 v67, v68, v69
	v_cvt_pk_f16_f32 v70, v70, v71
	v_cvt_pk_f16_f32 v71, v72, v73
	v_cvt_pk_f16_f32 v74, v74, v75
	v_cvt_pk_f16_f32 v75, v76, v77
	v_cvt_pk_f16_f32 v78, v78, v79
	v_cvt_pk_f16_f32 v79, v80, v81
	v_cvt_pk_f16_f32 v82, v82, v83
	v_cvt_pk_f16_f32 v83, v84, v85
	v_cvt_pk_f16_f32 v86, v86, v87
	v_cvt_pk_f16_f32 v87, v88, v89
	v_cvt_pk_f16_f32 v90, v90, v91
	v_cvt_pk_f16_f32 v91, v92, v93
	v_cvt_pk_f16_f32 v94, v94, v95
	v_cvt_pk_f16_f32 v95, v96, v97
	ds_write_b64 v134, v[66:67] offset:16384
	ds_write_b64 v135, v[70:71] offset:16384
	ds_write_b64 v139, v[74:75] offset:16896
	ds_write_b64 v139, v[78:79] offset:17152
	ds_write_b64 v1, v[82:83] offset:16384
	ds_write_b64 v136, v[86:87] offset:16384
	ds_write_b64 v137, v[90:91] offset:16384
	ds_write_b64 v138, v[94:95] offset:16384
	s_add_u32 s22, s30, s28
	s_addc_u32 s23, s31, 0
	global_load_dwordx4 v[66:69], v204, s[22:23] nt
	global_load_dwordx4 v[70:73], v205, s[22:23] nt
	global_load_dwordx4 v[74:77], v206, s[22:23] nt
	global_load_dwordx4 v[78:81], v207, s[22:23] nt
	global_load_dwordx4 v[82:85], v208, s[22:23] nt
	global_load_dwordx4 v[86:89], v209, s[22:23] nt
	global_load_dwordx4 v[90:93], v210, s[22:23] nt
	global_load_dwordx4 v[94:97], v211, s[22:23] nt
	s_addk_i32 s28, 0x100
	s_and_b32 s28, s28, 0x1fff
	s_waitcnt lgkmcnt(0)
	s_barrier
	s_waitcnt vmcnt(40)
	v_cvt_pk_f16_f32 v98, v98, v99
	v_cvt_pk_f16_f32 v99, v100, v101
	v_cvt_pk_f16_f32 v102, v102, v103
	v_cvt_pk_f16_f32 v103, v104, v105
	v_cvt_pk_f16_f32 v106, v106, v107
	v_cvt_pk_f16_f32 v107, v108, v109
	v_cvt_pk_f16_f32 v110, v110, v111
	v_cvt_pk_f16_f32 v111, v112, v113
	v_cvt_pk_f16_f32 v114, v114, v115
	v_cvt_pk_f16_f32 v115, v116, v117
	v_cvt_pk_f16_f32 v118, v118, v119
	v_cvt_pk_f16_f32 v119, v120, v121
	v_cvt_pk_f16_f32 v122, v122, v123
	v_cvt_pk_f16_f32 v123, v124, v125
	v_cvt_pk_f16_f32 v126, v126, v127
	v_cvt_pk_f16_f32 v127, v128, v129
	ds_write_b64 v134, v[98:99]
	ds_write_b64 v135, v[102:103]
	ds_write_b64 v139, v[106:107] offset:512
	ds_write_b64 v139, v[110:111] offset:768
	ds_write_b64 v1, v[114:115]
	ds_write_b64 v136, v[118:119]
	ds_write_b64 v137, v[122:123]
	ds_write_b64 v138, v[126:127]
	s_add_u32 s22, s30, s28
	s_addc_u32 s23, s31, 0
	global_load_dwordx4 v[98:101], v204, s[22:23] nt
	global_load_dwordx4 v[102:105], v205, s[22:23] nt
	global_load_dwordx4 v[106:109], v206, s[22:23] nt
	global_load_dwordx4 v[110:113], v207, s[22:23] nt
	global_load_dwordx4 v[114:117], v208, s[22:23] nt
	global_load_dwordx4 v[118:121], v209, s[22:23] nt
	global_load_dwordx4 v[122:125], v210, s[22:23] nt
	global_load_dwordx4 v[126:129], v211, s[22:23] nt
	s_addk_i32 s28, 0x100
	s_and_b32 s28, s28, 0x1fff
	s_waitcnt lgkmcnt(0)
	s_barrier
	s_waitcnt vmcnt(40)
	v_cvt_pk_f16_f32 v140, v140, v141
	v_cvt_pk_f16_f32 v141, v142, v143
	v_cvt_pk_f16_f32 v144, v144, v145
	v_cvt_pk_f16_f32 v145, v146, v147
	v_cvt_pk_f16_f32 v148, v148, v149
	v_cvt_pk_f16_f32 v149, v150, v151
	v_cvt_pk_f16_f32 v152, v152, v153
	v_cvt_pk_f16_f32 v153, v154, v155
	v_cvt_pk_f16_f32 v156, v156, v157
	v_cvt_pk_f16_f32 v157, v158, v159
	v_cvt_pk_f16_f32 v160, v160, v161
	v_cvt_pk_f16_f32 v161, v162, v163
	v_cvt_pk_f16_f32 v164, v164, v165
	v_cvt_pk_f16_f32 v165, v166, v167
	v_cvt_pk_f16_f32 v168, v168, v169
	v_cvt_pk_f16_f32 v169, v170, v171
	ds_write_b64 v134, v[140:141] offset:8192
	ds_write_b64 v135, v[144:145] offset:8192
	ds_write_b64 v139, v[148:149] offset:8704
	ds_write_b64 v139, v[152:153] offset:8960
	ds_write_b64 v1, v[156:157] offset:8192
	ds_write_b64 v136, v[160:161] offset:8192
	ds_write_b64 v137, v[164:165] offset:8192
	ds_write_b64 v138, v[168:169] offset:8192
	s_add_u32 s22, s30, s28
	s_addc_u32 s23, s31, 0
	global_load_dwordx4 v[140:143], v204, s[22:23] nt
	global_load_dwordx4 v[144:147], v205, s[22:23] nt
	global_load_dwordx4 v[148:151], v206, s[22:23] nt
	global_load_dwordx4 v[152:155], v207, s[22:23] nt
	global_load_dwordx4 v[156:159], v208, s[22:23] nt
	global_load_dwordx4 v[160:163], v209, s[22:23] nt
	global_load_dwordx4 v[164:167], v210, s[22:23] nt
	global_load_dwordx4 v[168:171], v211, s[22:23] nt
	s_addk_i32 s28, 0x100
	s_and_b32 s28, s28, 0x1fff
	s_waitcnt lgkmcnt(0)
	s_barrier
	s_waitcnt vmcnt(40)
	v_cvt_pk_f16_f32 v172, v172, v173
	v_cvt_pk_f16_f32 v173, v174, v175
	v_cvt_pk_f16_f32 v176, v176, v177
	v_cvt_pk_f16_f32 v177, v178, v179
	v_cvt_pk_f16_f32 v180, v180, v181
	v_cvt_pk_f16_f32 v181, v182, v183
	v_cvt_pk_f16_f32 v184, v184, v185
	v_cvt_pk_f16_f32 v185, v186, v187
	v_cvt_pk_f16_f32 v188, v188, v189
	v_cvt_pk_f16_f32 v189, v190, v191
	v_cvt_pk_f16_f32 v192, v192, v193
	v_cvt_pk_f16_f32 v193, v194, v195
	v_cvt_pk_f16_f32 v196, v196, v197
	v_cvt_pk_f16_f32 v197, v198, v199
	v_cvt_pk_f16_f32 v200, v200, v201
	v_cvt_pk_f16_f32 v201, v202, v203
	ds_write_b64 v134, v[172:173] offset:16384
	ds_write_b64 v135, v[176:177] offset:16384
	ds_write_b64 v139, v[180:181] offset:16896
	ds_write_b64 v139, v[184:185] offset:17152
	ds_write_b64 v1, v[188:189] offset:16384
	ds_write_b64 v136, v[192:193] offset:16384
	ds_write_b64 v137, v[196:197] offset:16384
	ds_write_b64 v138, v[200:201] offset:16384
	s_add_u32 s22, s30, s28
	s_addc_u32 s23, s31, 0
	global_load_dwordx4 v[172:175], v204, s[22:23] nt
	global_load_dwordx4 v[176:179], v205, s[22:23] nt
	global_load_dwordx4 v[180:183], v206, s[22:23] nt
	global_load_dwordx4 v[184:187], v207, s[22:23] nt
	global_load_dwordx4 v[188:191], v208, s[22:23] nt
	global_load_dwordx4 v[192:195], v209, s[22:23] nt
	global_load_dwordx4 v[196:199], v210, s[22:23] nt
	global_load_dwordx4 v[200:203], v211, s[22:23] nt
	s_addk_i32 s28, 0x100
	s_and_b32 s28, s28, 0x1fff
	s_waitcnt lgkmcnt(0)
	s_barrier
	s_waitcnt vmcnt(40)
	v_cvt_pk_f16_f32 v2, v2, v3
	v_cvt_pk_f16_f32 v3, v4, v5
	v_cvt_pk_f16_f32 v6, v6, v7
	v_cvt_pk_f16_f32 v7, v8, v9
	v_cvt_pk_f16_f32 v10, v10, v11
	v_cvt_pk_f16_f32 v11, v12, v13
	v_cvt_pk_f16_f32 v14, v14, v15
	v_cvt_pk_f16_f32 v15, v16, v17
	v_cvt_pk_f16_f32 v18, v18, v19
	v_cvt_pk_f16_f32 v19, v20, v21
	v_cvt_pk_f16_f32 v22, v22, v23
	v_cvt_pk_f16_f32 v23, v24, v25
	v_cvt_pk_f16_f32 v26, v26, v27
	v_cvt_pk_f16_f32 v27, v28, v29
	v_cvt_pk_f16_f32 v30, v30, v31
	v_cvt_pk_f16_f32 v31, v32, v33
	ds_write_b64 v134, v[2:3]
	ds_write_b64 v135, v[6:7]
	ds_write_b64 v139, v[10:11] offset:512
	ds_write_b64 v139, v[14:15] offset:768
	ds_write_b64 v1, v[18:19]
	ds_write_b64 v136, v[22:23]
	ds_write_b64 v137, v[26:27]
	ds_write_b64 v138, v[30:31]
	s_add_u32 s22, s30, s28
	s_addc_u32 s23, s31, 0
	global_load_dwordx4 v[2:5], v204, s[22:23] nt
	global_load_dwordx4 v[6:9], v205, s[22:23] nt
	global_load_dwordx4 v[10:13], v206, s[22:23] nt
	global_load_dwordx4 v[14:17], v207, s[22:23] nt
	global_load_dwordx4 v[18:21], v208, s[22:23] nt
	global_load_dwordx4 v[22:25], v209, s[22:23] nt
	global_load_dwordx4 v[26:29], v210, s[22:23] nt
	global_load_dwordx4 v[30:33], v211, s[22:23] nt
	s_addk_i32 s28, 0x100
	s_and_b32 s28, s28, 0x1fff
	s_waitcnt lgkmcnt(0)
	s_barrier
	s_waitcnt vmcnt(40)
	v_cvt_pk_f16_f32 v34, v34, v35
	v_cvt_pk_f16_f32 v35, v36, v37
	v_cvt_pk_f16_f32 v38, v38, v39
	v_cvt_pk_f16_f32 v39, v40, v41
	v_cvt_pk_f16_f32 v42, v42, v43
	v_cvt_pk_f16_f32 v43, v44, v45
	v_cvt_pk_f16_f32 v46, v46, v47
	v_cvt_pk_f16_f32 v47, v48, v49
	v_cvt_pk_f16_f32 v50, v50, v51
	v_cvt_pk_f16_f32 v51, v52, v53
	v_cvt_pk_f16_f32 v54, v54, v55
	v_cvt_pk_f16_f32 v55, v56, v57
	v_cvt_pk_f16_f32 v58, v58, v59
	v_cvt_pk_f16_f32 v59, v60, v61
	v_cvt_pk_f16_f32 v62, v62, v63
	v_cvt_pk_f16_f32 v63, v64, v65
	ds_write_b64 v134, v[34:35] offset:8192
	ds_write_b64 v135, v[38:39] offset:8192
	ds_write_b64 v139, v[42:43] offset:8704
	ds_write_b64 v139, v[46:47] offset:8960
	ds_write_b64 v1, v[50:51] offset:8192
	ds_write_b64 v136, v[54:55] offset:8192
	ds_write_b64 v137, v[58:59] offset:8192
	ds_write_b64 v138, v[62:63] offset:8192
	s_add_u32 s22, s30, s28
	s_addc_u32 s23, s31, 0
	global_load_dwordx4 v[34:37], v204, s[22:23] nt
	global_load_dwordx4 v[38:41], v205, s[22:23] nt
	global_load_dwordx4 v[42:45], v206, s[22:23] nt
	global_load_dwordx4 v[46:49], v207, s[22:23] nt
	global_load_dwordx4 v[50:53], v208, s[22:23] nt
	global_load_dwordx4 v[54:57], v209, s[22:23] nt
	global_load_dwordx4 v[58:61], v210, s[22:23] nt
	global_load_dwordx4 v[62:65], v211, s[22:23] nt
	s_addk_i32 s28, 0x100
	s_and_b32 s28, s28, 0x1fff
	s_waitcnt lgkmcnt(0)
	s_barrier
	s_waitcnt vmcnt(40)
	v_cvt_pk_f16_f32 v66, v66, v67
	v_cvt_pk_f16_f32 v67, v68, v69
	v_cvt_pk_f16_f32 v70, v70, v71
	v_cvt_pk_f16_f32 v71, v72, v73
	v_cvt_pk_f16_f32 v74, v74, v75
	v_cvt_pk_f16_f32 v75, v76, v77
	v_cvt_pk_f16_f32 v78, v78, v79
	v_cvt_pk_f16_f32 v79, v80, v81
	v_cvt_pk_f16_f32 v82, v82, v83
	v_cvt_pk_f16_f32 v83, v84, v85
	v_cvt_pk_f16_f32 v86, v86, v87
	v_cvt_pk_f16_f32 v87, v88, v89
	v_cvt_pk_f16_f32 v90, v90, v91
	v_cvt_pk_f16_f32 v91, v92, v93
	v_cvt_pk_f16_f32 v94, v94, v95
	v_cvt_pk_f16_f32 v95, v96, v97
	ds_write_b64 v134, v[66:67] offset:16384
	ds_write_b64 v135, v[70:71] offset:16384
	ds_write_b64 v139, v[74:75] offset:16896
	ds_write_b64 v139, v[78:79] offset:17152
	ds_write_b64 v1, v[82:83] offset:16384
	ds_write_b64 v136, v[86:87] offset:16384
	ds_write_b64 v137, v[90:91] offset:16384
	ds_write_b64 v138, v[94:95] offset:16384
	s_add_u32 s22, s30, s28
	s_addc_u32 s23, s31, 0
	global_load_dwordx4 v[66:69], v204, s[22:23] nt
	global_load_dwordx4 v[70:73], v205, s[22:23] nt
	global_load_dwordx4 v[74:77], v206, s[22:23] nt
	global_load_dwordx4 v[78:81], v207, s[22:23] nt
	global_load_dwordx4 v[82:85], v208, s[22:23] nt
	global_load_dwordx4 v[86:89], v209, s[22:23] nt
	global_load_dwordx4 v[90:93], v210, s[22:23] nt
	global_load_dwordx4 v[94:97], v211, s[22:23] nt
	s_addk_i32 s28, 0x100
	s_and_b32 s28, s28, 0x1fff
	s_waitcnt lgkmcnt(0)
	s_barrier
	s_waitcnt vmcnt(40)
	v_cvt_pk_f16_f32 v98, v98, v99
	v_cvt_pk_f16_f32 v99, v100, v101
	v_cvt_pk_f16_f32 v102, v102, v103
	v_cvt_pk_f16_f32 v103, v104, v105
	v_cvt_pk_f16_f32 v106, v106, v107
	v_cvt_pk_f16_f32 v107, v108, v109
	v_cvt_pk_f16_f32 v110, v110, v111
	v_cvt_pk_f16_f32 v111, v112, v113
	v_cvt_pk_f16_f32 v114, v114, v115
	v_cvt_pk_f16_f32 v115, v116, v117
	v_cvt_pk_f16_f32 v118, v118, v119
	v_cvt_pk_f16_f32 v119, v120, v121
	v_cvt_pk_f16_f32 v122, v122, v123
	v_cvt_pk_f16_f32 v123, v124, v125
	v_cvt_pk_f16_f32 v126, v126, v127
	v_cvt_pk_f16_f32 v127, v128, v129
	ds_write_b64 v134, v[98:99]
	ds_write_b64 v135, v[102:103]
	ds_write_b64 v139, v[106:107] offset:512
	ds_write_b64 v139, v[110:111] offset:768
	ds_write_b64 v1, v[114:115]
	ds_write_b64 v136, v[118:119]
	ds_write_b64 v137, v[122:123]
	ds_write_b64 v138, v[126:127]
	s_add_u32 s22, s30, s28
	s_addc_u32 s23, s31, 0
	global_load_dwordx4 v[98:101], v204, s[22:23] nt
	global_load_dwordx4 v[102:105], v205, s[22:23] nt
	global_load_dwordx4 v[106:109], v206, s[22:23] nt
	global_load_dwordx4 v[110:113], v207, s[22:23] nt
	global_load_dwordx4 v[114:117], v208, s[22:23] nt
	global_load_dwordx4 v[118:121], v209, s[22:23] nt
	global_load_dwordx4 v[122:125], v210, s[22:23] nt
	global_load_dwordx4 v[126:129], v211, s[22:23] nt
	s_addk_i32 s28, 0x100
	s_and_b32 s28, s28, 0x1fff
	s_waitcnt lgkmcnt(0)
	s_barrier
	s_waitcnt vmcnt(40)
	v_cvt_pk_f16_f32 v140, v140, v141
	v_cvt_pk_f16_f32 v141, v142, v143
	v_cvt_pk_f16_f32 v144, v144, v145
	v_cvt_pk_f16_f32 v145, v146, v147
	v_cvt_pk_f16_f32 v148, v148, v149
	v_cvt_pk_f16_f32 v149, v150, v151
	v_cvt_pk_f16_f32 v152, v152, v153
	v_cvt_pk_f16_f32 v153, v154, v155
	v_cvt_pk_f16_f32 v156, v156, v157
	v_cvt_pk_f16_f32 v157, v158, v159
	v_cvt_pk_f16_f32 v160, v160, v161
	v_cvt_pk_f16_f32 v161, v162, v163
	v_cvt_pk_f16_f32 v164, v164, v165
	v_cvt_pk_f16_f32 v165, v166, v167
	v_cvt_pk_f16_f32 v168, v168, v169
	v_cvt_pk_f16_f32 v169, v170, v171
	ds_write_b64 v134, v[140:141] offset:8192
	ds_write_b64 v135, v[144:145] offset:8192
	ds_write_b64 v139, v[148:149] offset:8704
	ds_write_b64 v139, v[152:153] offset:8960
	ds_write_b64 v1, v[156:157] offset:8192
	ds_write_b64 v136, v[160:161] offset:8192
	ds_write_b64 v137, v[164:165] offset:8192
	ds_write_b64 v138, v[168:169] offset:8192
	s_add_u32 s22, s30, s28
	s_addc_u32 s23, s31, 0
	global_load_dwordx4 v[140:143], v204, s[22:23] nt
	global_load_dwordx4 v[144:147], v205, s[22:23] nt
	global_load_dwordx4 v[148:151], v206, s[22:23] nt
	global_load_dwordx4 v[152:155], v207, s[22:23] nt
	global_load_dwordx4 v[156:159], v208, s[22:23] nt
	global_load_dwordx4 v[160:163], v209, s[22:23] nt
	global_load_dwordx4 v[164:167], v210, s[22:23] nt
	global_load_dwordx4 v[168:171], v211, s[22:23] nt
	s_addk_i32 s28, 0x100
	s_and_b32 s28, s28, 0x1fff
	s_waitcnt lgkmcnt(0)
	s_barrier
	s_waitcnt vmcnt(40)
	v_cvt_pk_f16_f32 v172, v172, v173
	v_cvt_pk_f16_f32 v173, v174, v175
	v_cvt_pk_f16_f32 v176, v176, v177
	v_cvt_pk_f16_f32 v177, v178, v179
	v_cvt_pk_f16_f32 v180, v180, v181
	v_cvt_pk_f16_f32 v181, v182, v183
	v_cvt_pk_f16_f32 v184, v184, v185
	v_cvt_pk_f16_f32 v185, v186, v187
	v_cvt_pk_f16_f32 v188, v188, v189
	v_cvt_pk_f16_f32 v189, v190, v191
	v_cvt_pk_f16_f32 v192, v192, v193
	v_cvt_pk_f16_f32 v193, v194, v195
	v_cvt_pk_f16_f32 v196, v196, v197
	v_cvt_pk_f16_f32 v197, v198, v199
	v_cvt_pk_f16_f32 v200, v200, v201
	v_cvt_pk_f16_f32 v201, v202, v203
	ds_write_b64 v134, v[172:173] offset:16384
	ds_write_b64 v135, v[176:177] offset:16384
	ds_write_b64 v139, v[180:181] offset:16896
	ds_write_b64 v139, v[184:185] offset:17152
	ds_write_b64 v1, v[188:189] offset:16384
	ds_write_b64 v136, v[192:193] offset:16384
	ds_write_b64 v137, v[196:197] offset:16384
	ds_write_b64 v138, v[200:201] offset:16384
	s_add_u32 s22, s30, s28
	s_addc_u32 s23, s31, 0
	global_load_dwordx4 v[172:175], v204, s[22:23] nt
	global_load_dwordx4 v[176:179], v205, s[22:23] nt
	global_load_dwordx4 v[180:183], v206, s[22:23] nt
	global_load_dwordx4 v[184:187], v207, s[22:23] nt
	global_load_dwordx4 v[188:191], v208, s[22:23] nt
	global_load_dwordx4 v[192:195], v209, s[22:23] nt
	global_load_dwordx4 v[196:199], v210, s[22:23] nt
	global_load_dwordx4 v[200:203], v211, s[22:23] nt
	s_addk_i32 s28, 0x100
	s_and_b32 s28, s28, 0x1fff
	s_waitcnt lgkmcnt(0)
	s_barrier
	s_waitcnt vmcnt(40)
	v_cvt_pk_f16_f32 v2, v2, v3
	v_cvt_pk_f16_f32 v3, v4, v5
	v_cvt_pk_f16_f32 v6, v6, v7
	v_cvt_pk_f16_f32 v7, v8, v9
	v_cvt_pk_f16_f32 v10, v10, v11
	v_cvt_pk_f16_f32 v11, v12, v13
	v_cvt_pk_f16_f32 v14, v14, v15
	v_cvt_pk_f16_f32 v15, v16, v17
	v_cvt_pk_f16_f32 v18, v18, v19
	v_cvt_pk_f16_f32 v19, v20, v21
	v_cvt_pk_f16_f32 v22, v22, v23
	v_cvt_pk_f16_f32 v23, v24, v25
	v_cvt_pk_f16_f32 v26, v26, v27
	v_cvt_pk_f16_f32 v27, v28, v29
	v_cvt_pk_f16_f32 v30, v30, v31
	v_cvt_pk_f16_f32 v31, v32, v33
	ds_write_b64 v134, v[2:3]
	ds_write_b64 v135, v[6:7]
	ds_write_b64 v139, v[10:11] offset:512
	ds_write_b64 v139, v[14:15] offset:768
	ds_write_b64 v1, v[18:19]
	ds_write_b64 v136, v[22:23]
	ds_write_b64 v137, v[26:27]
	ds_write_b64 v138, v[30:31]
	s_add_u32 s22, s30, s28
	s_addc_u32 s23, s31, 0
	global_load_dwordx4 v[2:5], v204, s[22:23] nt
	global_load_dwordx4 v[6:9], v205, s[22:23] nt
	global_load_dwordx4 v[10:13], v206, s[22:23] nt
	global_load_dwordx4 v[14:17], v207, s[22:23] nt
	global_load_dwordx4 v[18:21], v208, s[22:23] nt
	global_load_dwordx4 v[22:25], v209, s[22:23] nt
	global_load_dwordx4 v[26:29], v210, s[22:23] nt
	global_load_dwordx4 v[30:33], v211, s[22:23] nt
	s_addk_i32 s28, 0x100
	s_and_b32 s28, s28, 0x1fff
	s_waitcnt lgkmcnt(0)
	s_barrier
	s_waitcnt vmcnt(40)
	v_cvt_pk_f16_f32 v34, v34, v35
	v_cvt_pk_f16_f32 v35, v36, v37
	v_cvt_pk_f16_f32 v38, v38, v39
	v_cvt_pk_f16_f32 v39, v40, v41
	v_cvt_pk_f16_f32 v42, v42, v43
	v_cvt_pk_f16_f32 v43, v44, v45
	v_cvt_pk_f16_f32 v46, v46, v47
	v_cvt_pk_f16_f32 v47, v48, v49
	v_cvt_pk_f16_f32 v50, v50, v51
	v_cvt_pk_f16_f32 v51, v52, v53
	v_cvt_pk_f16_f32 v54, v54, v55
	v_cvt_pk_f16_f32 v55, v56, v57
	v_cvt_pk_f16_f32 v58, v58, v59
	v_cvt_pk_f16_f32 v59, v60, v61
	v_cvt_pk_f16_f32 v62, v62, v63
	v_cvt_pk_f16_f32 v63, v64, v65
	ds_write_b64 v134, v[34:35] offset:8192
	ds_write_b64 v135, v[38:39] offset:8192
	ds_write_b64 v139, v[42:43] offset:8704
	ds_write_b64 v139, v[46:47] offset:8960
	ds_write_b64 v1, v[50:51] offset:8192
	ds_write_b64 v136, v[54:55] offset:8192
	ds_write_b64 v137, v[58:59] offset:8192
	ds_write_b64 v138, v[62:63] offset:8192
	s_add_u32 s22, s30, s28
	s_addc_u32 s23, s31, 0
	global_load_dwordx4 v[34:37], v204, s[22:23] nt
	global_load_dwordx4 v[38:41], v205, s[22:23] nt
	global_load_dwordx4 v[42:45], v206, s[22:23] nt
	global_load_dwordx4 v[46:49], v207, s[22:23] nt
	global_load_dwordx4 v[50:53], v208, s[22:23] nt
	global_load_dwordx4 v[54:57], v209, s[22:23] nt
	global_load_dwordx4 v[58:61], v210, s[22:23] nt
	global_load_dwordx4 v[62:65], v211, s[22:23] nt
	s_addk_i32 s28, 0x100
	s_and_b32 s28, s28, 0x1fff
	s_waitcnt lgkmcnt(0)
	s_barrier
	s_waitcnt vmcnt(40)
	v_cvt_pk_f16_f32 v66, v66, v67
	v_cvt_pk_f16_f32 v67, v68, v69
	v_cvt_pk_f16_f32 v70, v70, v71
	v_cvt_pk_f16_f32 v71, v72, v73
	v_cvt_pk_f16_f32 v74, v74, v75
	v_cvt_pk_f16_f32 v75, v76, v77
	v_cvt_pk_f16_f32 v78, v78, v79
	v_cvt_pk_f16_f32 v79, v80, v81
	v_cvt_pk_f16_f32 v82, v82, v83
	v_cvt_pk_f16_f32 v83, v84, v85
	v_cvt_pk_f16_f32 v86, v86, v87
	v_cvt_pk_f16_f32 v87, v88, v89
	v_cvt_pk_f16_f32 v90, v90, v91
	v_cvt_pk_f16_f32 v91, v92, v93
	v_cvt_pk_f16_f32 v94, v94, v95
	v_cvt_pk_f16_f32 v95, v96, v97
	ds_write_b64 v134, v[66:67] offset:16384
	ds_write_b64 v135, v[70:71] offset:16384
	ds_write_b64 v139, v[74:75] offset:16896
	ds_write_b64 v139, v[78:79] offset:17152
	ds_write_b64 v1, v[82:83] offset:16384
	ds_write_b64 v136, v[86:87] offset:16384
	ds_write_b64 v137, v[90:91] offset:16384
	ds_write_b64 v138, v[94:95] offset:16384
	s_add_u32 s22, s30, s28
	s_addc_u32 s23, s31, 0
	global_load_dwordx4 v[66:69], v204, s[22:23] nt
	global_load_dwordx4 v[70:73], v205, s[22:23] nt
	global_load_dwordx4 v[74:77], v206, s[22:23] nt
	global_load_dwordx4 v[78:81], v207, s[22:23] nt
	global_load_dwordx4 v[82:85], v208, s[22:23] nt
	global_load_dwordx4 v[86:89], v209, s[22:23] nt
	global_load_dwordx4 v[90:93], v210, s[22:23] nt
	global_load_dwordx4 v[94:97], v211, s[22:23] nt
	s_addk_i32 s28, 0x100
	s_and_b32 s28, s28, 0x1fff
	s_waitcnt lgkmcnt(0)
	s_barrier
	s_waitcnt vmcnt(40)
	v_cvt_pk_f16_f32 v98, v98, v99
	v_cvt_pk_f16_f32 v99, v100, v101
	v_cvt_pk_f16_f32 v102, v102, v103
	v_cvt_pk_f16_f32 v103, v104, v105
	v_cvt_pk_f16_f32 v106, v106, v107
	v_cvt_pk_f16_f32 v107, v108, v109
	v_cvt_pk_f16_f32 v110, v110, v111
	v_cvt_pk_f16_f32 v111, v112, v113
	v_cvt_pk_f16_f32 v114, v114, v115
	v_cvt_pk_f16_f32 v115, v116, v117
	v_cvt_pk_f16_f32 v118, v118, v119
	v_cvt_pk_f16_f32 v119, v120, v121
	v_cvt_pk_f16_f32 v122, v122, v123
	v_cvt_pk_f16_f32 v123, v124, v125
	v_cvt_pk_f16_f32 v126, v126, v127
	v_cvt_pk_f16_f32 v127, v128, v129
	ds_write_b64 v134, v[98:99]
	ds_write_b64 v135, v[102:103]
	ds_write_b64 v139, v[106:107] offset:512
	ds_write_b64 v139, v[110:111] offset:768
	ds_write_b64 v1, v[114:115]
	ds_write_b64 v136, v[118:119]
	ds_write_b64 v137, v[122:123]
	ds_write_b64 v138, v[126:127]
	s_add_u32 s22, s30, s28
	s_addc_u32 s23, s31, 0
	global_load_dwordx4 v[98:101], v204, s[22:23] nt
	global_load_dwordx4 v[102:105], v205, s[22:23] nt
	global_load_dwordx4 v[106:109], v206, s[22:23] nt
	global_load_dwordx4 v[110:113], v207, s[22:23] nt
	global_load_dwordx4 v[114:117], v208, s[22:23] nt
	global_load_dwordx4 v[118:121], v209, s[22:23] nt
	global_load_dwordx4 v[122:125], v210, s[22:23] nt
	global_load_dwordx4 v[126:129], v211, s[22:23] nt
	s_addk_i32 s28, 0x100
	s_and_b32 s28, s28, 0x1fff
	s_waitcnt lgkmcnt(0)
	s_barrier
	s_waitcnt vmcnt(40)
	v_cvt_pk_f16_f32 v140, v140, v141
	v_cvt_pk_f16_f32 v141, v142, v143
	v_cvt_pk_f16_f32 v144, v144, v145
	v_cvt_pk_f16_f32 v145, v146, v147
	v_cvt_pk_f16_f32 v148, v148, v149
	v_cvt_pk_f16_f32 v149, v150, v151
	v_cvt_pk_f16_f32 v152, v152, v153
	v_cvt_pk_f16_f32 v153, v154, v155
	v_cvt_pk_f16_f32 v156, v156, v157
	v_cvt_pk_f16_f32 v157, v158, v159
	v_cvt_pk_f16_f32 v160, v160, v161
	v_cvt_pk_f16_f32 v161, v162, v163
	v_cvt_pk_f16_f32 v164, v164, v165
	v_cvt_pk_f16_f32 v165, v166, v167
	v_cvt_pk_f16_f32 v168, v168, v169
	v_cvt_pk_f16_f32 v169, v170, v171
	ds_write_b64 v134, v[140:141] offset:8192
	ds_write_b64 v135, v[144:145] offset:8192
	ds_write_b64 v139, v[148:149] offset:8704
	ds_write_b64 v139, v[152:153] offset:8960
	ds_write_b64 v1, v[156:157] offset:8192
	ds_write_b64 v136, v[160:161] offset:8192
	ds_write_b64 v137, v[164:165] offset:8192
	ds_write_b64 v138, v[168:169] offset:8192
	s_add_u32 s22, s30, s28
	s_addc_u32 s23, s31, 0
	global_load_dwordx4 v[140:143], v204, s[22:23] nt
	global_load_dwordx4 v[144:147], v205, s[22:23] nt
	global_load_dwordx4 v[148:151], v206, s[22:23] nt
	global_load_dwordx4 v[152:155], v207, s[22:23] nt
	global_load_dwordx4 v[156:159], v208, s[22:23] nt
	global_load_dwordx4 v[160:163], v209, s[22:23] nt
	global_load_dwordx4 v[164:167], v210, s[22:23] nt
	global_load_dwordx4 v[168:171], v211, s[22:23] nt
	s_addk_i32 s28, 0x100
	s_and_b32 s28, s28, 0x1fff
	s_waitcnt lgkmcnt(0)
	s_barrier
	s_waitcnt vmcnt(40)
	v_cvt_pk_f16_f32 v172, v172, v173
	v_cvt_pk_f16_f32 v173, v174, v175
	v_cvt_pk_f16_f32 v176, v176, v177
	v_cvt_pk_f16_f32 v177, v178, v179
	v_cvt_pk_f16_f32 v180, v180, v181
	v_cvt_pk_f16_f32 v181, v182, v183
	v_cvt_pk_f16_f32 v184, v184, v185
	v_cvt_pk_f16_f32 v185, v186, v187
	v_cvt_pk_f16_f32 v188, v188, v189
	v_cvt_pk_f16_f32 v189, v190, v191
	v_cvt_pk_f16_f32 v192, v192, v193
	v_cvt_pk_f16_f32 v193, v194, v195
	v_cvt_pk_f16_f32 v196, v196, v197
	v_cvt_pk_f16_f32 v197, v198, v199
	v_cvt_pk_f16_f32 v200, v200, v201
	v_cvt_pk_f16_f32 v201, v202, v203
	ds_write_b64 v134, v[172:173] offset:16384
	ds_write_b64 v135, v[176:177] offset:16384
	ds_write_b64 v139, v[180:181] offset:16896
	ds_write_b64 v139, v[184:185] offset:17152
	ds_write_b64 v1, v[188:189] offset:16384
	ds_write_b64 v136, v[192:193] offset:16384
	ds_write_b64 v137, v[196:197] offset:16384
	ds_write_b64 v138, v[200:201] offset:16384
	s_add_u32 s22, s30, s28
	s_addc_u32 s23, s31, 0
	global_load_dwordx4 v[172:175], v204, s[22:23] nt
	global_load_dwordx4 v[176:179], v205, s[22:23] nt
	global_load_dwordx4 v[180:183], v206, s[22:23] nt
	global_load_dwordx4 v[184:187], v207, s[22:23] nt
	global_load_dwordx4 v[188:191], v208, s[22:23] nt
	global_load_dwordx4 v[192:195], v209, s[22:23] nt
	global_load_dwordx4 v[196:199], v210, s[22:23] nt
	global_load_dwordx4 v[200:203], v211, s[22:23] nt
	s_addk_i32 s28, 0x100
	s_and_b32 s28, s28, 0x1fff
	s_waitcnt lgkmcnt(0)
	s_barrier
	s_waitcnt vmcnt(40)
	v_cvt_pk_f16_f32 v2, v2, v3
	v_cvt_pk_f16_f32 v3, v4, v5
	v_cvt_pk_f16_f32 v6, v6, v7
	v_cvt_pk_f16_f32 v7, v8, v9
	v_cvt_pk_f16_f32 v10, v10, v11
	v_cvt_pk_f16_f32 v11, v12, v13
	v_cvt_pk_f16_f32 v14, v14, v15
	v_cvt_pk_f16_f32 v15, v16, v17
	v_cvt_pk_f16_f32 v18, v18, v19
	v_cvt_pk_f16_f32 v19, v20, v21
	v_cvt_pk_f16_f32 v22, v22, v23
	v_cvt_pk_f16_f32 v23, v24, v25
	v_cvt_pk_f16_f32 v26, v26, v27
	v_cvt_pk_f16_f32 v27, v28, v29
	v_cvt_pk_f16_f32 v30, v30, v31
	v_cvt_pk_f16_f32 v31, v32, v33
	ds_write_b64 v134, v[2:3]
	ds_write_b64 v135, v[6:7]
	ds_write_b64 v139, v[10:11] offset:512
	ds_write_b64 v139, v[14:15] offset:768
	ds_write_b64 v1, v[18:19]
	ds_write_b64 v136, v[22:23]
	ds_write_b64 v137, v[26:27]
	ds_write_b64 v138, v[30:31]
	s_add_u32 s22, s30, s28
	s_addc_u32 s23, s31, 0
	global_load_dwordx4 v[2:5], v204, s[22:23] nt
	global_load_dwordx4 v[6:9], v205, s[22:23] nt
	global_load_dwordx4 v[10:13], v206, s[22:23] nt
	global_load_dwordx4 v[14:17], v207, s[22:23] nt
	global_load_dwordx4 v[18:21], v208, s[22:23] nt
	global_load_dwordx4 v[22:25], v209, s[22:23] nt
	global_load_dwordx4 v[26:29], v210, s[22:23] nt
	global_load_dwordx4 v[30:33], v211, s[22:23] nt
	s_addk_i32 s28, 0x100
	s_and_b32 s28, s28, 0x1fff
	s_waitcnt lgkmcnt(0)
	s_barrier
	s_waitcnt vmcnt(40)
	v_cvt_pk_f16_f32 v34, v34, v35
	v_cvt_pk_f16_f32 v35, v36, v37
	v_cvt_pk_f16_f32 v38, v38, v39
	v_cvt_pk_f16_f32 v39, v40, v41
	v_cvt_pk_f16_f32 v42, v42, v43
	v_cvt_pk_f16_f32 v43, v44, v45
	v_cvt_pk_f16_f32 v46, v46, v47
	v_cvt_pk_f16_f32 v47, v48, v49
	v_cvt_pk_f16_f32 v50, v50, v51
	v_cvt_pk_f16_f32 v51, v52, v53
	v_cvt_pk_f16_f32 v54, v54, v55
	v_cvt_pk_f16_f32 v55, v56, v57
	v_cvt_pk_f16_f32 v58, v58, v59
	v_cvt_pk_f16_f32 v59, v60, v61
	v_cvt_pk_f16_f32 v62, v62, v63
	v_cvt_pk_f16_f32 v63, v64, v65
	ds_write_b64 v134, v[34:35] offset:8192
	ds_write_b64 v135, v[38:39] offset:8192
	ds_write_b64 v139, v[42:43] offset:8704
	ds_write_b64 v139, v[46:47] offset:8960
	ds_write_b64 v1, v[50:51] offset:8192
	ds_write_b64 v136, v[54:55] offset:8192
	ds_write_b64 v137, v[58:59] offset:8192
	ds_write_b64 v138, v[62:63] offset:8192
	s_add_u32 s22, s30, s28
	s_addc_u32 s23, s31, 0
	global_load_dwordx4 v[34:37], v204, s[22:23] nt
	global_load_dwordx4 v[38:41], v205, s[22:23] nt
	global_load_dwordx4 v[42:45], v206, s[22:23] nt
	global_load_dwordx4 v[46:49], v207, s[22:23] nt
	global_load_dwordx4 v[50:53], v208, s[22:23] nt
	global_load_dwordx4 v[54:57], v209, s[22:23] nt
	global_load_dwordx4 v[58:61], v210, s[22:23] nt
	global_load_dwordx4 v[62:65], v211, s[22:23] nt
	s_addk_i32 s28, 0x100
	s_and_b32 s28, s28, 0x1fff
	s_waitcnt lgkmcnt(0)
	s_barrier
	s_waitcnt vmcnt(40)
	v_cvt_pk_f16_f32 v66, v66, v67
	v_cvt_pk_f16_f32 v67, v68, v69
	v_cvt_pk_f16_f32 v70, v70, v71
	v_cvt_pk_f16_f32 v71, v72, v73
	v_cvt_pk_f16_f32 v74, v74, v75
	v_cvt_pk_f16_f32 v75, v76, v77
	v_cvt_pk_f16_f32 v78, v78, v79
	v_cvt_pk_f16_f32 v79, v80, v81
	v_cvt_pk_f16_f32 v82, v82, v83
	v_cvt_pk_f16_f32 v83, v84, v85
	v_cvt_pk_f16_f32 v86, v86, v87
	v_cvt_pk_f16_f32 v87, v88, v89
	v_cvt_pk_f16_f32 v90, v90, v91
	v_cvt_pk_f16_f32 v91, v92, v93
	v_cvt_pk_f16_f32 v94, v94, v95
	v_cvt_pk_f16_f32 v95, v96, v97
	ds_write_b64 v134, v[66:67] offset:16384
	ds_write_b64 v135, v[70:71] offset:16384
	ds_write_b64 v139, v[74:75] offset:16896
	ds_write_b64 v139, v[78:79] offset:17152
	ds_write_b64 v1, v[82:83] offset:16384
	ds_write_b64 v136, v[86:87] offset:16384
	ds_write_b64 v137, v[90:91] offset:16384
	ds_write_b64 v138, v[94:95] offset:16384
	s_add_u32 s22, s30, s28
	s_addc_u32 s23, s31, 0
	global_load_dwordx4 v[66:69], v204, s[22:23] nt
	global_load_dwordx4 v[70:73], v205, s[22:23] nt
	global_load_dwordx4 v[74:77], v206, s[22:23] nt
	global_load_dwordx4 v[78:81], v207, s[22:23] nt
	global_load_dwordx4 v[82:85], v208, s[22:23] nt
	global_load_dwordx4 v[86:89], v209, s[22:23] nt
	global_load_dwordx4 v[90:93], v210, s[22:23] nt
	global_load_dwordx4 v[94:97], v211, s[22:23] nt
	s_addk_i32 s28, 0x100
	s_and_b32 s28, s28, 0x1fff
	s_waitcnt lgkmcnt(0)
	s_barrier
	s_waitcnt vmcnt(40)
	v_cvt_pk_f16_f32 v98, v98, v99
	v_cvt_pk_f16_f32 v99, v100, v101
	v_cvt_pk_f16_f32 v102, v102, v103
	v_cvt_pk_f16_f32 v103, v104, v105
	v_cvt_pk_f16_f32 v106, v106, v107
	v_cvt_pk_f16_f32 v107, v108, v109
	v_cvt_pk_f16_f32 v110, v110, v111
	v_cvt_pk_f16_f32 v111, v112, v113
	v_cvt_pk_f16_f32 v114, v114, v115
	v_cvt_pk_f16_f32 v115, v116, v117
	v_cvt_pk_f16_f32 v118, v118, v119
	v_cvt_pk_f16_f32 v119, v120, v121
	v_cvt_pk_f16_f32 v122, v122, v123
	v_cvt_pk_f16_f32 v123, v124, v125
	v_cvt_pk_f16_f32 v126, v126, v127
	v_cvt_pk_f16_f32 v127, v128, v129
	ds_write_b64 v134, v[98:99]
	ds_write_b64 v135, v[102:103]
	ds_write_b64 v139, v[106:107] offset:512
	ds_write_b64 v139, v[110:111] offset:768
	ds_write_b64 v1, v[114:115]
	ds_write_b64 v136, v[118:119]
	ds_write_b64 v137, v[122:123]
	ds_write_b64 v138, v[126:127]
	s_add_u32 s22, s30, s28
	s_addc_u32 s23, s31, 0
	global_load_dwordx4 v[98:101], v204, s[22:23] nt
	global_load_dwordx4 v[102:105], v205, s[22:23] nt
	global_load_dwordx4 v[106:109], v206, s[22:23] nt
	global_load_dwordx4 v[110:113], v207, s[22:23] nt
	global_load_dwordx4 v[114:117], v208, s[22:23] nt
	global_load_dwordx4 v[118:121], v209, s[22:23] nt
	global_load_dwordx4 v[122:125], v210, s[22:23] nt
	global_load_dwordx4 v[126:129], v211, s[22:23] nt
	s_addk_i32 s28, 0x100
	s_and_b32 s28, s28, 0x1fff
	s_waitcnt lgkmcnt(0)
	s_barrier
	s_waitcnt vmcnt(40)
	v_cvt_pk_f16_f32 v140, v140, v141
	v_cvt_pk_f16_f32 v141, v142, v143
	v_cvt_pk_f16_f32 v144, v144, v145
	v_cvt_pk_f16_f32 v145, v146, v147
	v_cvt_pk_f16_f32 v148, v148, v149
	v_cvt_pk_f16_f32 v149, v150, v151
	v_cvt_pk_f16_f32 v152, v152, v153
	v_cvt_pk_f16_f32 v153, v154, v155
	v_cvt_pk_f16_f32 v156, v156, v157
	v_cvt_pk_f16_f32 v157, v158, v159
	v_cvt_pk_f16_f32 v160, v160, v161
	v_cvt_pk_f16_f32 v161, v162, v163
	v_cvt_pk_f16_f32 v164, v164, v165
	v_cvt_pk_f16_f32 v165, v166, v167
	v_cvt_pk_f16_f32 v168, v168, v169
	v_cvt_pk_f16_f32 v169, v170, v171
	ds_write_b64 v134, v[140:141] offset:8192
	ds_write_b64 v135, v[144:145] offset:8192
	ds_write_b64 v139, v[148:149] offset:8704
	ds_write_b64 v139, v[152:153] offset:8960
	ds_write_b64 v1, v[156:157] offset:8192
	ds_write_b64 v136, v[160:161] offset:8192
	ds_write_b64 v137, v[164:165] offset:8192
	ds_write_b64 v138, v[168:169] offset:8192
	s_add_u32 s22, s30, s28
	s_addc_u32 s23, s31, 0
	global_load_dwordx4 v[140:143], v204, s[22:23] nt
	global_load_dwordx4 v[144:147], v205, s[22:23] nt
	global_load_dwordx4 v[148:151], v206, s[22:23] nt
	global_load_dwordx4 v[152:155], v207, s[22:23] nt
	global_load_dwordx4 v[156:159], v208, s[22:23] nt
	global_load_dwordx4 v[160:163], v209, s[22:23] nt
	global_load_dwordx4 v[164:167], v210, s[22:23] nt
	global_load_dwordx4 v[168:171], v211, s[22:23] nt
	s_addk_i32 s28, 0x100
	s_and_b32 s28, s28, 0x1fff
	s_waitcnt lgkmcnt(0)
	s_barrier
	s_waitcnt vmcnt(40)
	v_cvt_pk_f16_f32 v172, v172, v173
	v_cvt_pk_f16_f32 v173, v174, v175
	v_cvt_pk_f16_f32 v176, v176, v177
	v_cvt_pk_f16_f32 v177, v178, v179
	v_cvt_pk_f16_f32 v180, v180, v181
	v_cvt_pk_f16_f32 v181, v182, v183
	v_cvt_pk_f16_f32 v184, v184, v185
	v_cvt_pk_f16_f32 v185, v186, v187
	v_cvt_pk_f16_f32 v188, v188, v189
	v_cvt_pk_f16_f32 v189, v190, v191
	v_cvt_pk_f16_f32 v192, v192, v193
	v_cvt_pk_f16_f32 v193, v194, v195
	v_cvt_pk_f16_f32 v196, v196, v197
	v_cvt_pk_f16_f32 v197, v198, v199
	v_cvt_pk_f16_f32 v200, v200, v201
	v_cvt_pk_f16_f32 v201, v202, v203
	ds_write_b64 v134, v[172:173] offset:16384
	ds_write_b64 v135, v[176:177] offset:16384
	ds_write_b64 v139, v[180:181] offset:16896
	ds_write_b64 v139, v[184:185] offset:17152
	ds_write_b64 v1, v[188:189] offset:16384
	ds_write_b64 v136, v[192:193] offset:16384
	ds_write_b64 v137, v[196:197] offset:16384
	ds_write_b64 v138, v[200:201] offset:16384
	s_add_u32 s22, s30, s28
	s_addc_u32 s23, s31, 0
	global_load_dwordx4 v[172:175], v204, s[22:23] nt
	global_load_dwordx4 v[176:179], v205, s[22:23] nt
	global_load_dwordx4 v[180:183], v206, s[22:23] nt
	global_load_dwordx4 v[184:187], v207, s[22:23] nt
	global_load_dwordx4 v[188:191], v208, s[22:23] nt
	global_load_dwordx4 v[192:195], v209, s[22:23] nt
	global_load_dwordx4 v[196:199], v210, s[22:23] nt
	global_load_dwordx4 v[200:203], v211, s[22:23] nt
	s_addk_i32 s28, 0x100
	s_and_b32 s28, s28, 0x1fff
	s_waitcnt lgkmcnt(0)
	s_barrier
	s_waitcnt vmcnt(40)
	v_cvt_pk_f16_f32 v2, v2, v3
	v_cvt_pk_f16_f32 v3, v4, v5
	v_cvt_pk_f16_f32 v6, v6, v7
	v_cvt_pk_f16_f32 v7, v8, v9
	v_cvt_pk_f16_f32 v10, v10, v11
	v_cvt_pk_f16_f32 v11, v12, v13
	v_cvt_pk_f16_f32 v14, v14, v15
	v_cvt_pk_f16_f32 v15, v16, v17
	v_cvt_pk_f16_f32 v18, v18, v19
	v_cvt_pk_f16_f32 v19, v20, v21
	v_cvt_pk_f16_f32 v22, v22, v23
	v_cvt_pk_f16_f32 v23, v24, v25
	v_cvt_pk_f16_f32 v26, v26, v27
	v_cvt_pk_f16_f32 v27, v28, v29
	v_cvt_pk_f16_f32 v30, v30, v31
	v_cvt_pk_f16_f32 v31, v32, v33
	ds_write_b64 v134, v[2:3]
	ds_write_b64 v135, v[6:7]
	ds_write_b64 v139, v[10:11] offset:512
	ds_write_b64 v139, v[14:15] offset:768
	ds_write_b64 v1, v[18:19]
	ds_write_b64 v136, v[22:23]
	ds_write_b64 v137, v[26:27]
	ds_write_b64 v138, v[30:31]
	s_add_u32 s22, s30, s28
	s_addc_u32 s23, s31, 0
	global_load_dwordx4 v[2:5], v204, s[22:23] nt
	global_load_dwordx4 v[6:9], v205, s[22:23] nt
	global_load_dwordx4 v[10:13], v206, s[22:23] nt
	global_load_dwordx4 v[14:17], v207, s[22:23] nt
	global_load_dwordx4 v[18:21], v208, s[22:23] nt
	global_load_dwordx4 v[22:25], v209, s[22:23] nt
	global_load_dwordx4 v[26:29], v210, s[22:23] nt
	global_load_dwordx4 v[30:33], v211, s[22:23] nt
	s_addk_i32 s28, 0x100
	s_and_b32 s28, s28, 0x1fff
	s_waitcnt lgkmcnt(0)
	s_barrier
	s_waitcnt vmcnt(40)
	v_cvt_pk_f16_f32 v34, v34, v35
	v_cvt_pk_f16_f32 v35, v36, v37
	v_cvt_pk_f16_f32 v38, v38, v39
	v_cvt_pk_f16_f32 v39, v40, v41
	v_cvt_pk_f16_f32 v42, v42, v43
	v_cvt_pk_f16_f32 v43, v44, v45
	v_cvt_pk_f16_f32 v46, v46, v47
	v_cvt_pk_f16_f32 v47, v48, v49
	v_cvt_pk_f16_f32 v50, v50, v51
	v_cvt_pk_f16_f32 v51, v52, v53
	v_cvt_pk_f16_f32 v54, v54, v55
	v_cvt_pk_f16_f32 v55, v56, v57
	v_cvt_pk_f16_f32 v58, v58, v59
	v_cvt_pk_f16_f32 v59, v60, v61
	v_cvt_pk_f16_f32 v62, v62, v63
	v_cvt_pk_f16_f32 v63, v64, v65
	ds_write_b64 v134, v[34:35] offset:8192
	ds_write_b64 v135, v[38:39] offset:8192
	ds_write_b64 v139, v[42:43] offset:8704
	ds_write_b64 v139, v[46:47] offset:8960
	ds_write_b64 v1, v[50:51] offset:8192
	ds_write_b64 v136, v[54:55] offset:8192
	ds_write_b64 v137, v[58:59] offset:8192
	ds_write_b64 v138, v[62:63] offset:8192
	s_add_u32 s22, s30, s28
	s_addc_u32 s23, s31, 0
	global_load_dwordx4 v[34:37], v204, s[22:23] nt
	global_load_dwordx4 v[38:41], v205, s[22:23] nt
	global_load_dwordx4 v[42:45], v206, s[22:23] nt
	global_load_dwordx4 v[46:49], v207, s[22:23] nt
	global_load_dwordx4 v[50:53], v208, s[22:23] nt
	global_load_dwordx4 v[54:57], v209, s[22:23] nt
	global_load_dwordx4 v[58:61], v210, s[22:23] nt
	global_load_dwordx4 v[62:65], v211, s[22:23] nt
	s_addk_i32 s28, 0x100
	s_and_b32 s28, s28, 0x1fff
	s_waitcnt lgkmcnt(0)
	s_barrier
	s_waitcnt vmcnt(40)
	v_cvt_pk_f16_f32 v66, v66, v67
	v_cvt_pk_f16_f32 v67, v68, v69
	v_cvt_pk_f16_f32 v70, v70, v71
	v_cvt_pk_f16_f32 v71, v72, v73
	v_cvt_pk_f16_f32 v74, v74, v75
	v_cvt_pk_f16_f32 v75, v76, v77
	v_cvt_pk_f16_f32 v78, v78, v79
	v_cvt_pk_f16_f32 v79, v80, v81
	v_cvt_pk_f16_f32 v82, v82, v83
	v_cvt_pk_f16_f32 v83, v84, v85
	v_cvt_pk_f16_f32 v86, v86, v87
	v_cvt_pk_f16_f32 v87, v88, v89
	v_cvt_pk_f16_f32 v90, v90, v91
	v_cvt_pk_f16_f32 v91, v92, v93
	v_cvt_pk_f16_f32 v94, v94, v95
	v_cvt_pk_f16_f32 v95, v96, v97
	ds_write_b64 v134, v[66:67] offset:16384
	ds_write_b64 v135, v[70:71] offset:16384
	ds_write_b64 v139, v[74:75] offset:16896
	ds_write_b64 v139, v[78:79] offset:17152
	ds_write_b64 v1, v[82:83] offset:16384
	ds_write_b64 v136, v[86:87] offset:16384
	ds_write_b64 v137, v[90:91] offset:16384
	ds_write_b64 v138, v[94:95] offset:16384
	s_waitcnt lgkmcnt(0)
	s_barrier
	s_waitcnt vmcnt(32)
	v_cvt_pk_f16_f32 v98, v98, v99
	v_cvt_pk_f16_f32 v99, v100, v101
	v_cvt_pk_f16_f32 v102, v102, v103
	v_cvt_pk_f16_f32 v103, v104, v105
	v_cvt_pk_f16_f32 v106, v106, v107
	v_cvt_pk_f16_f32 v107, v108, v109
	v_cvt_pk_f16_f32 v110, v110, v111
	v_cvt_pk_f16_f32 v111, v112, v113
	v_cvt_pk_f16_f32 v114, v114, v115
	v_cvt_pk_f16_f32 v115, v116, v117
	v_cvt_pk_f16_f32 v118, v118, v119
	v_cvt_pk_f16_f32 v119, v120, v121
	v_cvt_pk_f16_f32 v122, v122, v123
	v_cvt_pk_f16_f32 v123, v124, v125
	v_cvt_pk_f16_f32 v126, v126, v127
	v_cvt_pk_f16_f32 v127, v128, v129
	ds_write_b64 v134, v[98:99]
	ds_write_b64 v135, v[102:103]
	ds_write_b64 v139, v[106:107] offset:512
	ds_write_b64 v139, v[110:111] offset:768
	ds_write_b64 v1, v[114:115]
	ds_write_b64 v136, v[118:119]
	ds_write_b64 v137, v[122:123]
	ds_write_b64 v138, v[126:127]
	s_waitcnt lgkmcnt(0)
	s_barrier
	s_waitcnt vmcnt(24)
	v_cvt_pk_f16_f32 v140, v140, v141
	v_cvt_pk_f16_f32 v141, v142, v143
	v_cvt_pk_f16_f32 v144, v144, v145
	v_cvt_pk_f16_f32 v145, v146, v147
	v_cvt_pk_f16_f32 v148, v148, v149
	v_cvt_pk_f16_f32 v149, v150, v151
	v_cvt_pk_f16_f32 v152, v152, v153
	v_cvt_pk_f16_f32 v153, v154, v155
	v_cvt_pk_f16_f32 v156, v156, v157
	v_cvt_pk_f16_f32 v157, v158, v159
	v_cvt_pk_f16_f32 v160, v160, v161
	v_cvt_pk_f16_f32 v161, v162, v163
	v_cvt_pk_f16_f32 v164, v164, v165
	v_cvt_pk_f16_f32 v165, v166, v167
	v_cvt_pk_f16_f32 v168, v168, v169
	v_cvt_pk_f16_f32 v169, v170, v171
	ds_write_b64 v134, v[140:141] offset:8192
	ds_write_b64 v135, v[144:145] offset:8192
	ds_write_b64 v139, v[148:149] offset:8704
	ds_write_b64 v139, v[152:153] offset:8960
	ds_write_b64 v1, v[156:157] offset:8192
	ds_write_b64 v136, v[160:161] offset:8192
	ds_write_b64 v137, v[164:165] offset:8192
	ds_write_b64 v138, v[168:169] offset:8192
	s_waitcnt lgkmcnt(0)
	s_barrier
	s_waitcnt vmcnt(16)
	v_cvt_pk_f16_f32 v172, v172, v173
	v_cvt_pk_f16_f32 v173, v174, v175
	v_cvt_pk_f16_f32 v176, v176, v177
	v_cvt_pk_f16_f32 v177, v178, v179
	v_cvt_pk_f16_f32 v180, v180, v181
	v_cvt_pk_f16_f32 v181, v182, v183
	v_cvt_pk_f16_f32 v184, v184, v185
	v_cvt_pk_f16_f32 v185, v186, v187
	v_cvt_pk_f16_f32 v188, v188, v189
	v_cvt_pk_f16_f32 v189, v190, v191
	v_cvt_pk_f16_f32 v192, v192, v193
	v_cvt_pk_f16_f32 v193, v194, v195
	v_cvt_pk_f16_f32 v196, v196, v197
	v_cvt_pk_f16_f32 v197, v198, v199
	v_cvt_pk_f16_f32 v200, v200, v201
	v_cvt_pk_f16_f32 v201, v202, v203
	ds_write_b64 v134, v[172:173] offset:16384
	ds_write_b64 v135, v[176:177] offset:16384
	ds_write_b64 v139, v[180:181] offset:16896
	ds_write_b64 v139, v[184:185] offset:17152
	ds_write_b64 v1, v[188:189] offset:16384
	ds_write_b64 v136, v[192:193] offset:16384
	ds_write_b64 v137, v[196:197] offset:16384
	ds_write_b64 v138, v[200:201] offset:16384
	s_waitcnt lgkmcnt(0)
	s_barrier
	s_waitcnt vmcnt(8)
	v_cvt_pk_f16_f32 v2, v2, v3
	v_cvt_pk_f16_f32 v3, v4, v5
	v_cvt_pk_f16_f32 v6, v6, v7
	v_cvt_pk_f16_f32 v7, v8, v9
	v_cvt_pk_f16_f32 v10, v10, v11
	v_cvt_pk_f16_f32 v11, v12, v13
	v_cvt_pk_f16_f32 v14, v14, v15
	v_cvt_pk_f16_f32 v15, v16, v17
	v_cvt_pk_f16_f32 v18, v18, v19
	v_cvt_pk_f16_f32 v19, v20, v21
	v_cvt_pk_f16_f32 v22, v22, v23
	v_cvt_pk_f16_f32 v23, v24, v25
	v_cvt_pk_f16_f32 v26, v26, v27
	v_cvt_pk_f16_f32 v27, v28, v29
	v_cvt_pk_f16_f32 v30, v30, v31
	v_cvt_pk_f16_f32 v31, v32, v33
	ds_write_b64 v134, v[2:3]
	ds_write_b64 v135, v[6:7]
	ds_write_b64 v139, v[10:11] offset:512
	ds_write_b64 v139, v[14:15] offset:768
	ds_write_b64 v1, v[18:19]
	ds_write_b64 v136, v[22:23]
	ds_write_b64 v137, v[26:27]
	ds_write_b64 v138, v[30:31]
	s_waitcnt lgkmcnt(0)
	s_barrier
	s_waitcnt vmcnt(0)
	v_cvt_pk_f16_f32 v34, v34, v35
	v_cvt_pk_f16_f32 v35, v36, v37
	v_cvt_pk_f16_f32 v38, v38, v39
	v_cvt_pk_f16_f32 v39, v40, v41
	v_cvt_pk_f16_f32 v42, v42, v43
	v_cvt_pk_f16_f32 v43, v44, v45
	v_cvt_pk_f16_f32 v46, v46, v47
	v_cvt_pk_f16_f32 v47, v48, v49
	v_cvt_pk_f16_f32 v50, v50, v51
	v_cvt_pk_f16_f32 v51, v52, v53
	v_cvt_pk_f16_f32 v54, v54, v55
	v_cvt_pk_f16_f32 v55, v56, v57
	v_cvt_pk_f16_f32 v58, v58, v59
	v_cvt_pk_f16_f32 v59, v60, v61
	v_cvt_pk_f16_f32 v62, v62, v63
	v_cvt_pk_f16_f32 v63, v64, v65
	ds_write_b64 v134, v[34:35] offset:8192
	ds_write_b64 v135, v[38:39] offset:8192
	ds_write_b64 v139, v[42:43] offset:8704
	ds_write_b64 v139, v[46:47] offset:8960
	ds_write_b64 v1, v[50:51] offset:8192
	ds_write_b64 v136, v[54:55] offset:8192
	ds_write_b64 v137, v[58:59] offset:8192
	ds_write_b64 v138, v[62:63] offset:8192
	s_waitcnt lgkmcnt(0)
	s_barrier

	.amdhsa_kernel _Z6kv1s_k5RArgs
		.amdhsa_group_segment_fixed_size 122880
		.amdhsa_private_segment_fixed_size 0
		.amdhsa_kernarg_size 88
		.amdhsa_user_sgpr_count 2
		.amdhsa_user_sgpr_dispatch_ptr 0
		.amdhsa_user_sgpr_queue_ptr 0
		.amdhsa_user_sgpr_kernarg_segment_ptr 1
		.amdhsa_user_sgpr_dispatch_id 0
		.amdhsa_user_sgpr_kernarg_preload_length 0
		.amdhsa_user_sgpr_kernarg_preload_offset 0
		.amdhsa_user_sgpr_private_segment_size 0
		.amdhsa_uses_dynamic_stack 0
		.amdhsa_enable_private_segment 0
		.amdhsa_system_sgpr_workgroup_id_x 1
		.amdhsa_system_sgpr_workgroup_id_y 0
		.amdhsa_system_sgpr_workgroup_id_z 0
		.amdhsa_system_sgpr_workgroup_info 0
		.amdhsa_system_vgpr_workitem_id 0
		.amdhsa_next_free_vgpr 212
		.amdhsa_next_free_sgpr 96
		.amdhsa_accum_offset 212
		.amdhsa_reserve_vcc 1
		.amdhsa_float_round_mode_32 0
		.amdhsa_float_round_mode_16_64 0
		.amdhsa_float_denorm_mode_32 3
		.amdhsa_float_denorm_mode_16_64 3
		.amdhsa_dx10_clamp 1
		.amdhsa_ieee_mode 1
		.amdhsa_fp16_overflow 0
		.amdhsa_tg_split 0
		.amdhsa_exception_fp_ieee_invalid_op 0
		.amdhsa_exception_fp_denorm_src 0
		.amdhsa_exception_fp_ieee_div_zero 0
		.amdhsa_exception_fp_ieee_overflow 0
		.amdhsa_exception_fp_ieee_underflow 0
		.amdhsa_exception_fp_ieee_inexact 0
		.amdhsa_exception_int_div_zero 0
	.end_amdhsa_kernel

.LBB6_26:
	s_ashr_i32 s0, s50, 4
	s_ashr_i32 s1, s0, 31
	s_lshl_b64 s[0:1], s[0:1], 24
	s_add_u32 s0, s8, s0
	s_addc_u32 s1, s9, s1
	s_lshl_b32 s2, s50, 10
	s_and_b32 s2, s2, 0x3c00
	s_add_u32 s0, s0, s2
	s_addc_u32 s1, s1, 0
	s_lshl_b32 s2, s62, 2
	s_add_u32 s2, s0, s2
	s_addc_u32 s3, s1, 0
	s_lshl_b32 s0, s49, 8
	s_add_i32 s0, s0, s56
	v_or_b32_e32 v86, s0, v134
	v_ashrrev_i32_e32 v87, 31, v86
	v_lshl_add_u64 v[86:87], v[86:87], 2, s[10:11]
	s_barrier
	global_load_dword v240, v[86:87], off
	global_load_dword v242, v[86:87], off offset:64
	global_load_dword v244, v[86:87], off offset:128
	global_load_dword v246, v[86:87], off offset:192
	global_load_dword v248, v[86:87], off offset:512
	global_load_dword v250, v[86:87], off offset:576
	global_load_dword v252, v[86:87], off offset:640
	global_load_dword v254, v[86:87], off offset:704
	s_mulk_i32 s43, 0x900
	v_bfe_u32 v87, v0, 3, 3
	v_and_b32_e32 v0, 7, v0
	v_mul_u32_u24_e32 v86, 0x90, v134
	v_add3_u32 v86, s43, v86, v1
	v_lshlrev_b32_e32 v138, 4, v0
	s_movk_i32 s1, 0x90
	v_or_b32_e32 v0, s43, v138
	v_mad_u32_u24 v88, v87, s1, v0
	v_mov_b32_e32 v139, 0
	v_or_b32_e32 v89, 8, v87
	v_lshl_add_u64 v[0:1], s[2:3], 0, v[138:139]
	v_or_b32_e32 v138, s0, v87
	v_mov_b32_e32 v135, v139
	v_or_b32_e32 v140, s0, v89
	v_ashrrev_i32_e32 v139, 31, v138
	v_ashrrev_i32_e32 v141, 31, v140
	v_lshlrev_b64 v[138:139], 14, v[138:139]
	v_lshlrev_b64 v[140:141], 14, v[140:141]
	v_lshl_add_u64 v[138:139], v[0:1], 0, v[138:139]
	v_lshl_add_u64 v[140:141], v[0:1], 0, v[140:141]
	s_ashr_i32 s1, s0, 31
	s_add_i32 s2, s0, 0x80
	s_waitcnt vmcnt(0)
	v_pk_add_f32 v[132:133], v[132:133], v[240:241] op_sel_hi:[1,0]
	v_pk_add_f32 v[130:131], v[130:131], v[240:241] op_sel_hi:[1,0]
	v_pk_add_f32 v[128:129], v[128:129], v[240:241] op_sel_hi:[1,0]
	v_pk_add_f32 v[126:127], v[126:127], v[240:241] op_sel_hi:[1,0]
	ds_write_b128 v86, v[130:133]
	ds_write_b128 v86, v[126:129] offset:64
	s_waitcnt lgkmcnt(0)
	ds_read_b128 v[126:129], v88
	ds_read_b128 v[130:133], v88 offset:1152
	v_pk_add_f32 v[124:125], v[124:125], v[240:241] op_sel_hi:[1,0]
	v_pk_add_f32 v[122:123], v[122:123], v[240:241] op_sel_hi:[1,0]
	s_waitcnt lgkmcnt(0)
	global_store_dwordx4 v[138:139], v[126:129], off nt
	global_store_dwordx4 v[140:141], v[130:133], off nt
	v_pk_add_f32 v[120:121], v[120:121], v[240:241] op_sel_hi:[1,0]
	v_pk_add_f32 v[118:119], v[118:119], v[240:241] op_sel_hi:[1,0]
	s_waitcnt lgkmcnt(0)
	ds_write_b128 v86, v[122:125]
	ds_write_b128 v86, v[118:121] offset:64
	s_waitcnt lgkmcnt(0)
	ds_read_b128 v[118:121], v88
	ds_read_b128 v[122:125], v88 offset:1152
	v_lshl_add_u64 v[126:127], s[0:1], 0, v[134:135]
	s_waitcnt lgkmcnt(1)
	global_store_dwordx4 v[138:139], v[118:121], off offset:512 nt
	s_waitcnt lgkmcnt(0)
	global_store_dwordx4 v[140:141], v[122:125], off offset:512 nt
	v_lshl_add_u64 v[126:127], v[126:127], 2, s[10:11]
	s_waitcnt lgkmcnt(0)
	s_or_b32 s1, s0, 16
	v_or_b32_e32 v120, s1, v87
	v_or_b32_e32 v122, s1, v89
	v_ashrrev_i32_e32 v121, 31, v120
	v_ashrrev_i32_e32 v123, 31, v122
	v_lshlrev_b64 v[120:121], 14, v[120:121]
	v_lshlrev_b64 v[122:123], 14, v[122:123]
	v_lshl_add_u64 v[120:121], v[0:1], 0, v[120:121]
	v_lshl_add_u64 v[122:123], v[0:1], 0, v[122:123]
	s_or_b32 s1, s0, 32
	v_pk_add_f32 v[116:117], v[116:117], v[242:243] op_sel_hi:[1,0]
	v_pk_add_f32 v[114:115], v[114:115], v[242:243] op_sel_hi:[1,0]
	v_pk_add_f32 v[112:113], v[112:113], v[242:243] op_sel_hi:[1,0]
	v_pk_add_f32 v[110:111], v[110:111], v[242:243] op_sel_hi:[1,0]
	ds_write_b128 v86, v[114:117]
	ds_write_b128 v86, v[110:113] offset:64
	s_waitcnt lgkmcnt(0)
	ds_read_b128 v[110:113], v88
	ds_read_b128 v[114:117], v88 offset:1152
	v_pk_add_f32 v[108:109], v[108:109], v[242:243] op_sel_hi:[1,0]
	v_pk_add_f32 v[106:107], v[106:107], v[242:243] op_sel_hi:[1,0]
	s_waitcnt lgkmcnt(1)
	global_store_dwordx4 v[120:121], v[110:113], off nt
	s_waitcnt lgkmcnt(0)
	global_store_dwordx4 v[122:123], v[114:117], off nt
	v_pk_add_f32 v[104:105], v[104:105], v[242:243] op_sel_hi:[1,0]
	v_pk_add_f32 v[102:103], v[102:103], v[242:243] op_sel_hi:[1,0]
	s_waitcnt lgkmcnt(0)
	ds_write_b128 v86, v[106:109]
	ds_write_b128 v86, v[102:105] offset:64
	s_waitcnt lgkmcnt(0)
	ds_read_b128 v[102:105], v88
	ds_read_b128 v[106:109], v88 offset:1152
	s_waitcnt lgkmcnt(1)
	global_store_dwordx4 v[120:121], v[102:105], off offset:512 nt
	s_waitcnt lgkmcnt(0)
	global_store_dwordx4 v[122:123], v[106:109], off offset:512 nt
	s_waitcnt lgkmcnt(0)
	v_or_b32_e32 v104, s1, v87
	v_or_b32_e32 v106, s1, v89
	v_ashrrev_i32_e32 v105, 31, v104
	v_ashrrev_i32_e32 v107, 31, v106
	v_lshlrev_b64 v[104:105], 14, v[104:105]
	v_lshlrev_b64 v[106:107], 14, v[106:107]
	v_lshl_add_u64 v[104:105], v[0:1], 0, v[104:105]
	v_lshl_add_u64 v[106:107], v[0:1], 0, v[106:107]
	s_or_b32 s1, s0, 48
	v_pk_add_f32 v[100:101], v[100:101], v[244:245] op_sel_hi:[1,0]
	v_pk_add_f32 v[98:99], v[98:99], v[244:245] op_sel_hi:[1,0]
	v_pk_add_f32 v[96:97], v[96:97], v[244:245] op_sel_hi:[1,0]
	v_pk_add_f32 v[94:95], v[94:95], v[244:245] op_sel_hi:[1,0]
	ds_write_b128 v86, v[98:101]
	ds_write_b128 v86, v[94:97] offset:64
	s_waitcnt lgkmcnt(0)
	ds_read_b128 v[94:97], v88
	ds_read_b128 v[98:101], v88 offset:1152
	v_pk_add_f32 v[92:93], v[92:93], v[244:245] op_sel_hi:[1,0]
	v_pk_add_f32 v[90:91], v[90:91], v[244:245] op_sel_hi:[1,0]
	s_waitcnt lgkmcnt(1)
	global_store_dwordx4 v[104:105], v[94:97], off nt
	s_waitcnt lgkmcnt(0)
	global_store_dwordx4 v[106:107], v[98:101], off nt
	v_pk_add_f32 v[84:85], v[84:85], v[244:245] op_sel_hi:[1,0]
	v_pk_add_f32 v[82:83], v[82:83], v[244:245] op_sel_hi:[1,0]
	s_waitcnt lgkmcnt(0)
	ds_write_b128 v86, v[90:93]
	ds_write_b128 v86, v[82:85] offset:64
	s_waitcnt lgkmcnt(0)
	ds_read_b128 v[82:85], v88
	ds_read_b128 v[90:93], v88 offset:1152
	s_waitcnt lgkmcnt(1)
	global_store_dwordx4 v[104:105], v[82:85], off offset:512 nt
	s_waitcnt lgkmcnt(0)
	global_store_dwordx4 v[106:107], v[90:93], off offset:512 nt
	s_waitcnt lgkmcnt(0)
	v_or_b32_e32 v84, s1, v87
	v_or_b32_e32 v90, s1, v89
	v_ashrrev_i32_e32 v85, 31, v84
	v_ashrrev_i32_e32 v91, 31, v90
	v_lshlrev_b64 v[84:85], 14, v[84:85]
	v_lshlrev_b64 v[90:91], 14, v[90:91]
	v_lshl_add_u64 v[84:85], v[0:1], 0, v[84:85]
	v_lshl_add_u64 v[90:91], v[0:1], 0, v[90:91]
	s_add_i32 s1, s0, 0x90
	v_pk_add_f32 v[80:81], v[80:81], v[246:247] op_sel_hi:[1,0]
	v_pk_add_f32 v[78:79], v[78:79], v[246:247] op_sel_hi:[1,0]
	v_pk_add_f32 v[76:77], v[76:77], v[246:247] op_sel_hi:[1,0]
	v_pk_add_f32 v[74:75], v[74:75], v[246:247] op_sel_hi:[1,0]
	ds_write_b128 v86, v[78:81]
	ds_write_b128 v86, v[74:77] offset:64
	s_waitcnt lgkmcnt(0)
	ds_read_b128 v[74:77], v88
	ds_read_b128 v[78:81], v88 offset:1152
	v_pk_add_f32 v[72:73], v[72:73], v[246:247] op_sel_hi:[1,0]
	v_pk_add_f32 v[70:71], v[70:71], v[246:247] op_sel_hi:[1,0]
	s_waitcnt lgkmcnt(1)
	global_store_dwordx4 v[84:85], v[74:77], off nt
	s_waitcnt lgkmcnt(0)
	global_store_dwordx4 v[90:91], v[78:81], off nt
	v_pk_add_f32 v[68:69], v[68:69], v[246:247] op_sel_hi:[1,0]
	v_pk_add_f32 v[66:67], v[66:67], v[246:247] op_sel_hi:[1,0]
	s_waitcnt lgkmcnt(0)
	ds_write_b128 v86, v[70:73]
	ds_write_b128 v86, v[66:69] offset:64
	s_waitcnt lgkmcnt(0)
	ds_read_b128 v[66:69], v88
	ds_read_b128 v[70:73], v88 offset:1152
	v_or_b32_e32 v74, s2, v134
	v_ashrrev_i32_e32 v75, 31, v74
	s_waitcnt lgkmcnt(1)
	global_store_dwordx4 v[84:85], v[66:69], off offset:512 nt
	s_waitcnt lgkmcnt(0)
	global_store_dwordx4 v[90:91], v[70:73], off offset:512 nt
	v_lshl_add_u64 v[74:75], v[74:75], 2, s[10:11]
	s_waitcnt lgkmcnt(0)
	v_or_b32_e32 v68, s2, v87
	v_or_b32_e32 v70, s2, v89
	v_ashrrev_i32_e32 v69, 31, v68
	v_ashrrev_i32_e32 v71, 31, v70
	v_lshlrev_b64 v[68:69], 14, v[68:69]
	v_lshlrev_b64 v[70:71], 14, v[70:71]
	v_lshl_add_u64 v[68:69], v[0:1], 0, v[68:69]
	v_lshl_add_u64 v[70:71], v[0:1], 0, v[70:71]
	s_add_i32 s2, s0, 0xa0
	s_addk_i32 s0, 0xb0
	v_pk_add_f32 v[64:65], v[64:65], v[248:249] op_sel_hi:[1,0]
	v_pk_add_f32 v[62:63], v[62:63], v[248:249] op_sel_hi:[1,0]
	v_pk_add_f32 v[60:61], v[60:61], v[248:249] op_sel_hi:[1,0]
	v_pk_add_f32 v[58:59], v[58:59], v[248:249] op_sel_hi:[1,0]
	ds_write_b128 v86, v[62:65]
	ds_write_b128 v86, v[58:61] offset:64
	s_waitcnt lgkmcnt(0)
	ds_read_b128 v[58:61], v88
	ds_read_b128 v[62:65], v88 offset:1152
	v_pk_add_f32 v[56:57], v[56:57], v[248:249] op_sel_hi:[1,0]
	v_pk_add_f32 v[54:55], v[54:55], v[248:249] op_sel_hi:[1,0]
	s_waitcnt lgkmcnt(1)
	global_store_dwordx4 v[68:69], v[58:61], off nt
	s_waitcnt lgkmcnt(0)
	global_store_dwordx4 v[70:71], v[62:65], off nt
	v_pk_add_f32 v[52:53], v[52:53], v[248:249] op_sel_hi:[1,0]
	v_pk_add_f32 v[50:51], v[50:51], v[248:249] op_sel_hi:[1,0]
	s_waitcnt lgkmcnt(0)
	ds_write_b128 v86, v[54:57]
	ds_write_b128 v86, v[50:53] offset:64
	s_waitcnt lgkmcnt(0)
	ds_read_b128 v[50:53], v88
	ds_read_b128 v[54:57], v88 offset:1152
	v_or_b32_e32 v58, s1, v134
	v_ashrrev_i32_e32 v59, 31, v58
	s_waitcnt lgkmcnt(1)
	global_store_dwordx4 v[68:69], v[50:53], off offset:512 nt
	s_waitcnt lgkmcnt(0)
	global_store_dwordx4 v[70:71], v[54:57], off offset:512 nt
	v_lshl_add_u64 v[58:59], v[58:59], 2, s[10:11]
	s_waitcnt lgkmcnt(0)
	v_or_b32_e32 v52, s1, v87
	v_or_b32_e32 v54, s1, v89
	v_ashrrev_i32_e32 v53, 31, v52
	v_ashrrev_i32_e32 v55, 31, v54
	v_lshlrev_b64 v[52:53], 14, v[52:53]
	v_lshlrev_b64 v[54:55], 14, v[54:55]
	v_lshl_add_u64 v[52:53], v[0:1], 0, v[52:53]
	v_lshl_add_u64 v[54:55], v[0:1], 0, v[54:55]
	v_pk_add_f32 v[48:49], v[48:49], v[250:251] op_sel_hi:[1,0]
	v_pk_add_f32 v[46:47], v[46:47], v[250:251] op_sel_hi:[1,0]
	v_pk_add_f32 v[44:45], v[44:45], v[250:251] op_sel_hi:[1,0]
	v_pk_add_f32 v[42:43], v[42:43], v[250:251] op_sel_hi:[1,0]
	ds_write_b128 v86, v[46:49]
	ds_write_b128 v86, v[42:45] offset:64
	s_waitcnt lgkmcnt(0)
	ds_read_b128 v[42:45], v88
	ds_read_b128 v[46:49], v88 offset:1152
	v_pk_add_f32 v[40:41], v[40:41], v[250:251] op_sel_hi:[1,0]
	v_pk_add_f32 v[38:39], v[38:39], v[250:251] op_sel_hi:[1,0]
	s_waitcnt lgkmcnt(1)
	global_store_dwordx4 v[52:53], v[42:45], off nt
	s_waitcnt lgkmcnt(0)
	global_store_dwordx4 v[54:55], v[46:49], off nt
	v_pk_add_f32 v[36:37], v[36:37], v[250:251] op_sel_hi:[1,0]
	v_pk_add_f32 v[34:35], v[34:35], v[250:251] op_sel_hi:[1,0]
	s_waitcnt lgkmcnt(0)
	ds_write_b128 v86, v[38:41]
	ds_write_b128 v86, v[34:37] offset:64
	s_waitcnt lgkmcnt(0)
	ds_read_b128 v[34:37], v88
	ds_read_b128 v[38:41], v88 offset:1152
	v_or_b32_e32 v42, s2, v134
	v_ashrrev_i32_e32 v43, 31, v42
	s_waitcnt lgkmcnt(1)
	global_store_dwordx4 v[52:53], v[34:37], off offset:512 nt
	s_waitcnt lgkmcnt(0)
	global_store_dwordx4 v[54:55], v[38:41], off offset:512 nt
	v_lshl_add_u64 v[42:43], v[42:43], 2, s[10:11]
	s_waitcnt lgkmcnt(0)
	v_or_b32_e32 v36, s2, v87
	v_or_b32_e32 v38, s2, v89
	v_ashrrev_i32_e32 v37, 31, v36
	v_ashrrev_i32_e32 v39, 31, v38
	v_lshlrev_b64 v[36:37], 14, v[36:37]
	v_lshlrev_b64 v[38:39], 14, v[38:39]
	v_lshl_add_u64 v[36:37], v[0:1], 0, v[36:37]
	v_lshl_add_u64 v[38:39], v[0:1], 0, v[38:39]
	v_pk_add_f32 v[32:33], v[32:33], v[252:253] op_sel_hi:[1,0]
	v_pk_add_f32 v[30:31], v[30:31], v[252:253] op_sel_hi:[1,0]
	v_pk_add_f32 v[28:29], v[28:29], v[252:253] op_sel_hi:[1,0]
	v_pk_add_f32 v[26:27], v[26:27], v[252:253] op_sel_hi:[1,0]
	ds_write_b128 v86, v[30:33]
	ds_write_b128 v86, v[26:29] offset:64
	s_waitcnt lgkmcnt(0)
	ds_read_b128 v[26:29], v88
	ds_read_b128 v[30:33], v88 offset:1152
	v_pk_add_f32 v[24:25], v[24:25], v[252:253] op_sel_hi:[1,0]
	v_pk_add_f32 v[22:23], v[22:23], v[252:253] op_sel_hi:[1,0]
	s_waitcnt lgkmcnt(1)
	global_store_dwordx4 v[36:37], v[26:29], off nt
	s_waitcnt lgkmcnt(0)
	global_store_dwordx4 v[38:39], v[30:33], off nt
	v_pk_add_f32 v[20:21], v[20:21], v[252:253] op_sel_hi:[1,0]
	v_pk_add_f32 v[18:19], v[18:19], v[252:253] op_sel_hi:[1,0]
	s_waitcnt lgkmcnt(0)
	ds_write_b128 v86, v[22:25]
	ds_write_b128 v86, v[18:21] offset:64
	s_waitcnt lgkmcnt(0)
	ds_read_b128 v[18:21], v88
	ds_read_b128 v[22:25], v88 offset:1152
	v_or_b32_e32 v26, s0, v134
	v_ashrrev_i32_e32 v27, 31, v26
	s_waitcnt lgkmcnt(1)
	global_store_dwordx4 v[36:37], v[18:21], off offset:512 nt
	s_waitcnt lgkmcnt(0)
	global_store_dwordx4 v[38:39], v[22:25], off offset:512 nt
	v_lshl_add_u64 v[26:27], v[26:27], 2, s[10:11]
	s_waitcnt lgkmcnt(0)
	v_or_b32_e32 v20, s0, v87
	v_or_b32_e32 v22, s0, v89
	v_ashrrev_i32_e32 v21, 31, v20
	v_ashrrev_i32_e32 v23, 31, v22
	v_lshlrev_b64 v[20:21], 14, v[20:21]
	v_lshlrev_b64 v[22:23], 14, v[22:23]
	v_lshl_add_u64 v[20:21], v[0:1], 0, v[20:21]
	v_lshl_add_u64 v[22:23], v[0:1], 0, v[22:23]
	v_pk_add_f32 v[16:17], v[16:17], v[254:255] op_sel_hi:[1,0]
	v_pk_add_f32 v[14:15], v[14:15], v[254:255] op_sel_hi:[1,0]
	v_pk_add_f32 v[12:13], v[12:13], v[254:255] op_sel_hi:[1,0]
	v_pk_add_f32 v[10:11], v[10:11], v[254:255] op_sel_hi:[1,0]
	ds_write_b128 v86, v[14:17]
	ds_write_b128 v86, v[10:13] offset:64
	s_waitcnt lgkmcnt(0)
	ds_read_b128 v[10:13], v88
	ds_read_b128 v[14:17], v88 offset:1152
	v_pk_add_f32 v[8:9], v[8:9], v[254:255] op_sel_hi:[1,0]
	v_pk_add_f32 v[6:7], v[6:7], v[254:255] op_sel_hi:[1,0]
	s_waitcnt lgkmcnt(1)
	global_store_dwordx4 v[20:21], v[10:13], off nt
	s_waitcnt lgkmcnt(0)
	global_store_dwordx4 v[22:23], v[14:17], off nt
	v_pk_add_f32 v[4:5], v[4:5], v[254:255] op_sel_hi:[1,0]
	v_pk_add_f32 v[2:3], v[2:3], v[254:255] op_sel_hi:[1,0]
	s_waitcnt lgkmcnt(0)
	ds_write_b128 v86, v[6:9]
	ds_write_b128 v86, v[2:5] offset:64
	s_waitcnt lgkmcnt(0)
	ds_read_b128 v[0:3], v88
	ds_read_b128 v[4:7], v88 offset:1152
	s_waitcnt lgkmcnt(1)
	global_store_dwordx4 v[20:21], v[0:3], off offset:512 nt
	s_waitcnt lgkmcnt(0)
	global_store_dwordx4 v[22:23], v[4:7], off offset:512 nt
	s_waitcnt lgkmcnt(0)

	.amdhsa_kernel _Z7k_phaseIN3pg86EpiOutEEvNS0_4GemmET_
		.amdhsa_group_segment_fixed_size 131072
		.amdhsa_private_segment_fixed_size 0
		.amdhsa_kernarg_size 304
		.amdhsa_user_sgpr_count 2
		.amdhsa_user_sgpr_dispatch_ptr 0
		.amdhsa_user_sgpr_queue_ptr 0
		.amdhsa_user_sgpr_kernarg_segment_ptr 1
		.amdhsa_user_sgpr_dispatch_id 0
		.amdhsa_user_sgpr_kernarg_preload_length 0
		.amdhsa_user_sgpr_kernarg_preload_offset 0
		.amdhsa_user_sgpr_private_segment_size 0
		.amdhsa_uses_dynamic_stack 0
		.amdhsa_enable_private_segment 0
		.amdhsa_system_sgpr_workgroup_id_x 1
		.amdhsa_system_sgpr_workgroup_id_y 0
		.amdhsa_system_sgpr_workgroup_id_z 0
		.amdhsa_system_sgpr_workgroup_info 0
		.amdhsa_system_vgpr_workitem_id 0
		.amdhsa_next_free_vgpr 256
		.amdhsa_next_free_sgpr 96
		.amdhsa_accum_offset 256
		.amdhsa_reserve_vcc 1
		.amdhsa_float_round_mode_32 0
		.amdhsa_float_round_mode_16_64 0
		.amdhsa_float_denorm_mode_32 3
		.amdhsa_float_denorm_mode_16_64 3
		.amdhsa_dx10_clamp 1
		.amdhsa_ieee_mode 1
		.amdhsa_fp16_overflow 0
		.amdhsa_tg_split 0
		.amdhsa_exception_fp_ieee_invalid_op 0
		.amdhsa_exception_fp_denorm_src 0
		.amdhsa_exception_fp_ieee_div_zero 0
		.amdhsa_exception_fp_ieee_overflow 0
		.amdhsa_exception_fp_ieee_underflow 0
		.amdhsa_exception_fp_ieee_inexact 0
		.amdhsa_exception_int_div_zero 0
	.end_amdhsa_kernel

amdhsa.kernels:
  - .agpr_count:     0
    .args:
      - .offset:         0
        .size:           120
        .value_kind:     by_value
    .group_segment_fixed_size: 16640
    .kernarg_segment_align: 8
    .kernarg_segment_size: 120
    .language:       OpenCL C
    .language_version:
      - 2
      - 0
    .max_flat_workgroup_size: 256
    .name:           _Z8prep_all5PArgs
    .private_segment_fixed_size: 0
    .sgpr_count:     45
    .sgpr_spill_count: 0
    .symbol:         _Z8prep_all5PArgs.kd
    .uniform_work_group_size: 1
    .uses_dynamic_stack: false
    .vgpr_count:     42
    .vgpr_spill_count: 0
    .wavefront_size: 64
  - .agpr_count:     0
    .args:
      - .actual_access:  read_only
        .address_space:  global
        .offset:         0
        .size:           8
        .value_kind:     global_buffer
      - .actual_access:  write_only
        .address_space:  global
        .offset:         8
        .size:           8
        .value_kind:     global_buffer
      - .actual_access:  read_only
        .address_space:  global
        .offset:         16
        .size:           8
        .value_kind:     global_buffer
      - .actual_access:  write_only
        .address_space:  global
        .offset:         24
        .size:           8
        .value_kind:     global_buffer
    .group_segment_fixed_size: 0
    .kernarg_segment_align: 8
    .kernarg_segment_size: 32
    .language:       OpenCL C
    .language_version:
      - 2
      - 0
    .max_flat_workgroup_size: 256
    .name:           _Z12reduce_slabsPKfPDF16_S0_Pf
    .private_segment_fixed_size: 0
    .sgpr_count:     17
    .sgpr_spill_count: 0
    .symbol:         _Z12reduce_slabsPKfPDF16_S0_Pf.kd
    .uniform_work_group_size: 1
    .uses_dynamic_stack: false
    .vgpr_count:     26
    .vgpr_spill_count: 0
    .wavefront_size: 64
  - .agpr_count:     0
    .args:
      - .offset:         0
        .size:           88
        .value_kind:     by_value
    .group_segment_fixed_size: 122880
    .kernarg_segment_align: 8
    .kernarg_segment_size: 88
    .language:       OpenCL C
    .language_version:
      - 2
      - 0
    .max_flat_workgroup_size: 512
    .name:           _Z6kv1s_k5RArgs
    .private_segment_fixed_size: 0
    .sgpr_count:     29
    .sgpr_spill_count: 0
    .symbol:         _Z6kv1s_k5RArgs.kd
    .uniform_work_group_size: 1
    .uses_dynamic_stack: false
    .vgpr_count:     212
    .vgpr_spill_count: 0
    .wavefront_size: 64
  - .agpr_count:     0
    .args:
      - .offset:         0
        .size:           88
        .value_kind:     by_value
      - .offset:         88
        .size:           32
        .value_kind:     by_value
      - .offset:         120
        .size:           16
        .value_kind:     by_value
    .group_segment_fixed_size: 131072
    .kernarg_segment_align: 8
    .kernarg_segment_size: 136
    .language:       OpenCL C
    .language_version:
      - 2
      - 0
    .max_flat_workgroup_size: 512
    .name:           _Z8k_kv2_qg5RArgsN3pg84GemmENS0_5EpiQTE
    .private_segment_fixed_size: 0
    .sgpr_count:     96
    .sgpr_spill_count: 0
    .symbol:         _Z8k_kv2_qg5RArgsN3pg84GemmENS0_5EpiQTE.kd
    .uniform_work_group_size: 1
    .uses_dynamic_stack: false
    .vgpr_count:     242
    .vgpr_spill_count: 0
    .wavefront_size: 64
  - .agpr_count:     0
    .args:
      - .offset:         0
        .size:           88
        .value_kind:     by_value
      - .offset:         88
        .size:           32
        .value_kind:     by_value
      - .offset:         120
        .size:           16
        .value_kind:     by_value
    .group_segment_fixed_size: 147456
    .kernarg_segment_align: 8
    .kernarg_segment_size: 136
    .language:       OpenCL C
    .language_version:
      - 2
      - 0
    .max_flat_workgroup_size: 512
    .name:           _Z8k_kv1_qg5RArgsN3pg84GemmENS0_5EpiQTE
    .private_segment_fixed_size: 0
    .sgpr_count:     82
    .sgpr_spill_count: 0
    .symbol:         _Z8k_kv1_qg5RArgsN3pg84GemmENS0_5EpiQTE.kd
    .uniform_work_group_size: 1
    .uses_dynamic_stack: false
    .vgpr_count:     242
    .vgpr_spill_count: 0
    .wavefront_size: 64
  - .agpr_count:     0
    .args:
      - .actual_access:  read_only
        .address_space:  global
        .offset:         0
        .size:           8
        .value_kind:     global_buffer
      - .actual_access:  read_only
        .address_space:  global
        .offset:         8
        .size:           8
        .value_kind:     global_buffer
      - .actual_access:  read_only
        .address_space:  global
        .offset:         16
        .size:           8
        .value_kind:     global_buffer
      - .actual_access:  write_only
        .address_space:  global
        .offset:         24
        .size:           8
        .value_kind:     global_buffer
    .group_segment_fixed_size: 102400
    .kernarg_segment_align: 8
    .kernarg_segment_size: 32
    .language:       OpenCL C
    .language_version:
      - 2
      - 0
    .max_flat_workgroup_size: 512
    .name:           _Z6attn_kPKDF16_S0_S0_PDF16_
    .private_segment_fixed_size: 0
    .sgpr_count:     19
    .sgpr_spill_count: 0
    .symbol:         _Z6attn_kPKDF16_S0_S0_PDF16_.kd
    .uniform_work_group_size: 1
    .uses_dynamic_stack: false
    .vgpr_count:     222
    .vgpr_spill_count: 0
    .wavefront_size: 64
  - .agpr_count:     0
    .args:
      - .offset:         0
        .size:           32
        .value_kind:     by_value
      - .offset:         32
        .size:           16
        .value_kind:     by_value
      - .offset:         48
        .size:           4
        .value_kind:     hidden_block_count_x
      - .offset:         52
        .size:           4
        .value_kind:     hidden_block_count_y
      - .offset:         56
        .size:           4
        .value_kind:     hidden_block_count_z
      - .offset:         60
        .size:           2
        .value_kind:     hidden_group_size_x
      - .offset:         62
        .size:           2
        .value_kind:     hidden_group_size_y
      - .offset:         64
        .size:           2
        .value_kind:     hidden_group_size_z
      - .offset:         66
        .size:           2
        .value_kind:     hidden_remainder_x
      - .offset:         68
        .size:           2
        .value_kind:     hidden_remainder_y
      - .offset:         70
        .size:           2
        .value_kind:     hidden_remainder_z
      - .offset:         88
        .size:           8
        .value_kind:     hidden_global_offset_x
      - .offset:         96
        .size:           8
        .value_kind:     hidden_global_offset_y
      - .offset:         104
        .size:           8
        .value_kind:     hidden_global_offset_z
      - .offset:         112
        .size:           2
        .value_kind:     hidden_grid_dims
    .group_segment_fixed_size: 131072
    .kernarg_segment_align: 8
    .kernarg_segment_size: 304
    .language:       OpenCL C
    .language_version:
      - 2
      - 0
    .max_flat_workgroup_size: 512
    .name:           _Z7k_phaseIN3pg86EpiOutEEvNS0_4GemmET_
    .private_segment_fixed_size: 0
    .sgpr_count:     84
    .sgpr_spill_count: 0
    .symbol:         _Z7k_phaseIN3pg86EpiOutEEvNS0_4GemmET_.kd
    .uniform_work_group_size: 1
    .uses_dynamic_stack: false
    .vgpr_count:     256
    .vgpr_spill_count: 0
    .wavefront_size: 64
